# snake chain order plus alternate chains issue k=1 before k=0 so consecutive MFMAs at chain boundaries share the same fragment registers (f32 accumulation order inside a K-tile changes for half of the
# baseline (speedup 1.0000x reference)
.LBB0_130:
	ds_read_b128 v[144:147], v140
	ds_read_b128 v[148:151], v140 offset:1024
	ds_read_b128 v[152:155], v140 offset:2048
	ds_read_b128 v[156:159], v140 offset:3072
	ds_read_b128 v[164:167], v141
	ds_read_b128 v[168:171], v141 offset:1024
	ds_read_b128 v[172:175], v141 offset:2048
	ds_read_b128 v[176:179], v141 offset:3072
	s_add_u32 s31, s10, 0xfff7c080
	s_addc_u32 s53, s11, -1
	s_cmp_eq_u32 s30, 28
	s_cselect_b32 s55, s25, s53
	s_cselect_b32 s54, s24, s31
	s_cselect_b32 s57, s4, s29
	s_cselect_b32 s56, s5, s28
	s_mov_b32 m0, s23
	ds_read_b128 v[180:183], v163
	ds_read_b128 v[190:193], v163 offset:1024
	ds_read_b128 v[194:197], v163 offset:2048
	ds_read_b128 v[198:201], v163 offset:3072
	ds_read_b128 v[202:205], v163 offset:4096
	ds_read_b128 v[206:209], v163 offset:5120
	ds_read_b128 v[216:219], v163 offset:6144
	ds_read_b128 v[220:223], v163 offset:7168
	global_load_lds_dwordx4 v138, s[10:11]
	s_mov_b32 m0, s33
	s_nop 0
	s_add_u32 s70, s10, s96
	s_addc_u32 s71, s11, s97
	global_load_lds_dwordx4 v138, s[70:71]
	s_waitcnt vmcnt(8)
	s_waitcnt lgkmcnt(0)
	s_barrier
	v_mfma_f32_16x16x32_bf16 v[120:123], v[144:147], v[180:183], v[120:123]
	v_mfma_f32_16x16x32_bf16 v[120:123], v[148:151], v[190:193], v[120:123]
	v_mfma_f32_16x16x32_bf16 v[116:119], v[156:159], v[190:193], v[116:119]
	v_mfma_f32_16x16x32_bf16 v[116:119], v[152:155], v[180:183], v[116:119]
	v_mfma_f32_16x16x32_bf16 v[128:131], v[164:167], v[180:183], v[128:131]
	v_mfma_f32_16x16x32_bf16 v[128:131], v[168:171], v[190:193], v[128:131]
	v_mfma_f32_16x16x32_bf16 v[124:127], v[176:179], v[190:193], v[124:127]
	v_mfma_f32_16x16x32_bf16 v[124:127], v[172:175], v[180:183], v[124:127]
	v_mfma_f32_16x16x32_bf16 v[108:111], v[172:175], v[194:197], v[108:111]
	v_mfma_f32_16x16x32_bf16 v[108:111], v[176:179], v[198:201], v[108:111]
	v_mfma_f32_16x16x32_bf16 v[112:115], v[168:171], v[198:201], v[112:115]
	v_mfma_f32_16x16x32_bf16 v[112:115], v[164:167], v[194:197], v[112:115]
	v_mfma_f32_16x16x32_bf16 v[100:103], v[152:155], v[194:197], v[100:103]
	v_mfma_f32_16x16x32_bf16 v[100:103], v[156:159], v[198:201], v[100:103]
	v_mfma_f32_16x16x32_bf16 v[104:107], v[148:151], v[198:201], v[104:107]
	v_mfma_f32_16x16x32_bf16 v[104:107], v[144:147], v[194:197], v[104:107]
	v_mfma_f32_16x16x32_bf16 v[88:91], v[144:147], v[202:205], v[88:91]
	v_mfma_f32_16x16x32_bf16 v[88:91], v[148:151], v[206:209], v[88:91]
	v_mfma_f32_16x16x32_bf16 v[84:87], v[156:159], v[206:209], v[84:87]
	v_mfma_f32_16x16x32_bf16 v[84:87], v[152:155], v[202:205], v[84:87]
	v_mfma_f32_16x16x32_bf16 v[96:99], v[164:167], v[202:205], v[96:99]
	v_mfma_f32_16x16x32_bf16 v[96:99], v[168:171], v[206:209], v[96:99]
	v_mfma_f32_16x16x32_bf16 v[92:95], v[176:179], v[206:209], v[92:95]
	v_mfma_f32_16x16x32_bf16 v[92:95], v[172:175], v[202:205], v[92:95]
	v_mfma_f32_16x16x32_bf16 v[76:79], v[172:175], v[216:219], v[76:79]
	v_mfma_f32_16x16x32_bf16 v[76:79], v[176:179], v[220:223], v[76:79]
	v_mfma_f32_16x16x32_bf16 v[80:83], v[168:171], v[220:223], v[80:83]
	v_mfma_f32_16x16x32_bf16 v[80:83], v[164:167], v[216:219], v[80:83]
	v_mfma_f32_16x16x32_bf16 v[68:71], v[152:155], v[216:219], v[68:71]
	v_mfma_f32_16x16x32_bf16 v[68:71], v[156:159], v[220:223], v[68:71]
	v_mfma_f32_16x16x32_bf16 v[72:75], v[148:151], v[220:223], v[72:75]
	v_mfma_f32_16x16x32_bf16 v[72:75], v[144:147], v[216:219], v[72:75]
	s_barrier
	s_mov_b32 m0, s45
	ds_read_b128 v[180:183], v163 offset:16384
	ds_read_b128 v[190:193], v163 offset:17408
	ds_read_b128 v[194:197], v163 offset:18432
	ds_read_b128 v[198:201], v163 offset:19456
	ds_read_b128 v[202:205], v163 offset:20480
	ds_read_b128 v[206:209], v163 offset:21504
	ds_read_b128 v[216:219], v163 offset:22528
	ds_read_b128 v[220:223], v163 offset:23552
	global_load_lds_dwordx4 v132, s[56:57]
	s_mov_b32 m0, s46
	s_nop 0
	s_add_u32 s70, s56, s90
	s_addc_u32 s71, s57, s91
	global_load_lds_dwordx4 v132, s[70:71]
	s_mov_b32 m0, s47
	s_nop 0
	s_add_u32 s70, s56, s60
	s_addc_u32 s71, s57, s61
	global_load_lds_dwordx4 v132, s[70:71]
	s_mov_b32 m0, s48
	s_nop 0
	s_add_u32 s70, s56, s64
	s_addc_u32 s71, s57, s65
	global_load_lds_dwordx4 v132, s[70:71]
	s_mov_b32 m0, s37
	s_nop 0
	global_load_lds_dwordx4 v134, s[54:55]
	s_mov_b32 m0, s38
	s_nop 0
	s_add_u32 s70, s54, s96
	s_addc_u32 s71, s55, s97
	global_load_lds_dwordx4 v134, s[70:71]
	s_waitcnt vmcnt(8)
	s_waitcnt lgkmcnt(0)
	s_barrier
	v_mfma_f32_16x16x32_bf16 v[56:59], v[144:147], v[180:183], v[56:59]
	v_mfma_f32_16x16x32_bf16 v[56:59], v[148:151], v[190:193], v[56:59]
	v_mfma_f32_16x16x32_bf16 v[52:55], v[156:159], v[190:193], v[52:55]
	v_mfma_f32_16x16x32_bf16 v[52:55], v[152:155], v[180:183], v[52:55]
	v_mfma_f32_16x16x32_bf16 v[64:67], v[164:167], v[180:183], v[64:67]
	v_mfma_f32_16x16x32_bf16 v[64:67], v[168:171], v[190:193], v[64:67]
	v_mfma_f32_16x16x32_bf16 v[60:63], v[176:179], v[190:193], v[60:63]
	v_mfma_f32_16x16x32_bf16 v[60:63], v[172:175], v[180:183], v[60:63]
	v_mfma_f32_16x16x32_bf16 v[44:47], v[172:175], v[194:197], v[44:47]
	v_mfma_f32_16x16x32_bf16 v[44:47], v[176:179], v[198:201], v[44:47]
	v_mfma_f32_16x16x32_bf16 v[48:51], v[168:171], v[198:201], v[48:51]
	v_mfma_f32_16x16x32_bf16 v[48:51], v[164:167], v[194:197], v[48:51]
	v_mfma_f32_16x16x32_bf16 v[36:39], v[152:155], v[194:197], v[36:39]
	v_mfma_f32_16x16x32_bf16 v[36:39], v[156:159], v[198:201], v[36:39]
	v_mfma_f32_16x16x32_bf16 v[40:43], v[148:151], v[198:201], v[40:43]
	v_mfma_f32_16x16x32_bf16 v[40:43], v[144:147], v[194:197], v[40:43]
	v_mfma_f32_16x16x32_bf16 v[24:27], v[144:147], v[202:205], v[24:27]
	v_mfma_f32_16x16x32_bf16 v[24:27], v[148:151], v[206:209], v[24:27]
	v_mfma_f32_16x16x32_bf16 v[20:23], v[156:159], v[206:209], v[20:23]
	v_mfma_f32_16x16x32_bf16 v[20:23], v[152:155], v[202:205], v[20:23]
	v_mfma_f32_16x16x32_bf16 v[32:35], v[164:167], v[202:205], v[32:35]
	v_mfma_f32_16x16x32_bf16 v[32:35], v[168:171], v[206:209], v[32:35]
	v_mfma_f32_16x16x32_bf16 v[28:31], v[176:179], v[206:209], v[28:31]
	v_mfma_f32_16x16x32_bf16 v[28:31], v[172:175], v[202:205], v[28:31]
	v_mfma_f32_16x16x32_bf16 v[12:15], v[172:175], v[216:219], v[12:15]
	v_mfma_f32_16x16x32_bf16 v[12:15], v[176:179], v[220:223], v[12:15]
	v_mfma_f32_16x16x32_bf16 v[16:19], v[168:171], v[220:223], v[16:19]
	v_mfma_f32_16x16x32_bf16 v[16:19], v[164:167], v[216:219], v[16:19]
	v_mfma_f32_16x16x32_bf16 v[4:7], v[152:155], v[216:219], v[4:7]
	v_mfma_f32_16x16x32_bf16 v[4:7], v[156:159], v[220:223], v[4:7]
	v_mfma_f32_16x16x32_bf16 v[8:11], v[148:151], v[220:223], v[8:11]
	v_mfma_f32_16x16x32_bf16 v[8:11], v[144:147], v[216:219], v[8:11]
	s_barrier
; #define PG8_MMA(ai, bj, At, Bt) do { __builtin_amdgcn_s_setprio(1); _Pragma("unroll") for (int m = 0; m < 4; ++m) _Pragma("unroll") for (int n = 0; n < 2; ++n) _Pragma("unroll") for (int k = 0; k < 2; ++k) \
;         acc[ai][bj][m][n] = __builtin_amdgcn_mfma_f32_16x16x32_bf16(Bt[n][k], At[m][k], acc[ai][bj][m][n], 0, 0, 0); __builtin_amdgcn_s_setprio(0); } while (0)
; #define PG8_WAIT_V(n) asm volatile("s_waitcnt vmcnt(" #n ")" ::: "memory")
; #define PG8_TRIP_HEAD(T) const int t = (T); const bool last = (t == nt - 2); \
;             const char* a1 = cA + (size_t)(t + 1) * kstep; \
;             const char* a2 = last ? nA : cA + (size_t)(t + 2) * kstep; const char* b2 = last ? nB : cB + (size_t)(t + 2) * kstep; \
;             const char* a3 = a2 + kstep; const char* b3 = b2 + kstep; \
;             if (last && has_next) S.a_ready(nxt);
; template <class Epi, class Sched, bool ALIGN_EPI = false, bool SP2 = false>
; __device__ __forceinline__ void gemm_phase(PG8_LAS unsigned char* lds, const Gemm g, const Sched& S, const Epi& E) {
;     ...
;         if constexpr (SP2) {
;             { PG8_TRIP_HEAD(0) PG8_TRIP_SP2(asm volatile("s_waitcnt vmcnt(%0)" :: "n"(8 + Epi::NST) : "memory"), PG8_MMAZ) }
;             for (int tt = 2; tt < nt; tt += 2) { PG8_TRIP_HEAD(tt) PG8_TRIP_SP2(PG8_WAIT_V(8), PG8_MMA) }
	ds_read_b128 v[144:147], v142
	ds_read_b128 v[148:151], v142 offset:1024
	ds_read_b128 v[152:155], v142 offset:2048
	ds_read_b128 v[156:159], v142 offset:3072
	ds_read_b128 v[164:167], v143
	ds_read_b128 v[168:171], v143 offset:1024
	ds_read_b128 v[172:175], v143 offset:2048
	ds_read_b128 v[176:179], v143 offset:3072
	s_mov_b32 m0, s39
	ds_read_b128 v[180:183], v163 offset:32768
	ds_read_b128 v[190:193], v163 offset:33792
	ds_read_b128 v[194:197], v163 offset:34816
	ds_read_b128 v[198:201], v163 offset:35840
	ds_read_b128 v[202:205], v163 offset:36864
	ds_read_b128 v[206:209], v163 offset:37888
	ds_read_b128 v[216:219], v163 offset:38912
	ds_read_b128 v[220:223], v163 offset:39936
	s_add_u32 s70, s54, s82
	s_addc_u32 s71, s55, s83
	global_load_lds_dwordx4 v134, s[70:71]
	s_mov_b32 m0, s40
	s_nop 0
	s_add_u32 s70, s54, s68
	s_addc_u32 s71, s55, s69
	global_load_lds_dwordx4 v134, s[70:71]
	s_waitcnt vmcnt(8)
	s_waitcnt lgkmcnt(0)
	s_barrier
	v_mfma_f32_16x16x32_bf16 v[120:123], v[144:147], v[180:183], v[120:123]
	v_mfma_f32_16x16x32_bf16 v[120:123], v[148:151], v[190:193], v[120:123]
	v_mfma_f32_16x16x32_bf16 v[116:119], v[156:159], v[190:193], v[116:119]
	v_mfma_f32_16x16x32_bf16 v[116:119], v[152:155], v[180:183], v[116:119]
	v_mfma_f32_16x16x32_bf16 v[128:131], v[164:167], v[180:183], v[128:131]
	v_mfma_f32_16x16x32_bf16 v[128:131], v[168:171], v[190:193], v[128:131]
	v_mfma_f32_16x16x32_bf16 v[124:127], v[176:179], v[190:193], v[124:127]
	v_mfma_f32_16x16x32_bf16 v[124:127], v[172:175], v[180:183], v[124:127]
	v_mfma_f32_16x16x32_bf16 v[108:111], v[172:175], v[194:197], v[108:111]
	v_mfma_f32_16x16x32_bf16 v[108:111], v[176:179], v[198:201], v[108:111]
	v_mfma_f32_16x16x32_bf16 v[112:115], v[168:171], v[198:201], v[112:115]
	v_mfma_f32_16x16x32_bf16 v[112:115], v[164:167], v[194:197], v[112:115]
	v_mfma_f32_16x16x32_bf16 v[100:103], v[152:155], v[194:197], v[100:103]
	v_mfma_f32_16x16x32_bf16 v[100:103], v[156:159], v[198:201], v[100:103]
	v_mfma_f32_16x16x32_bf16 v[104:107], v[148:151], v[198:201], v[104:107]
	v_mfma_f32_16x16x32_bf16 v[104:107], v[144:147], v[194:197], v[104:107]
	v_mfma_f32_16x16x32_bf16 v[88:91], v[144:147], v[202:205], v[88:91]
	v_mfma_f32_16x16x32_bf16 v[88:91], v[148:151], v[206:209], v[88:91]
	v_mfma_f32_16x16x32_bf16 v[84:87], v[156:159], v[206:209], v[84:87]
	v_mfma_f32_16x16x32_bf16 v[84:87], v[152:155], v[202:205], v[84:87]
	v_mfma_f32_16x16x32_bf16 v[96:99], v[164:167], v[202:205], v[96:99]
	v_mfma_f32_16x16x32_bf16 v[96:99], v[168:171], v[206:209], v[96:99]
	v_mfma_f32_16x16x32_bf16 v[92:95], v[176:179], v[206:209], v[92:95]
	v_mfma_f32_16x16x32_bf16 v[92:95], v[172:175], v[202:205], v[92:95]
	v_mfma_f32_16x16x32_bf16 v[76:79], v[172:175], v[216:219], v[76:79]
	v_mfma_f32_16x16x32_bf16 v[76:79], v[176:179], v[220:223], v[76:79]
	v_mfma_f32_16x16x32_bf16 v[80:83], v[168:171], v[220:223], v[80:83]
	v_mfma_f32_16x16x32_bf16 v[80:83], v[164:167], v[216:219], v[80:83]
	v_mfma_f32_16x16x32_bf16 v[68:71], v[152:155], v[216:219], v[68:71]
	v_mfma_f32_16x16x32_bf16 v[68:71], v[156:159], v[220:223], v[68:71]
	v_mfma_f32_16x16x32_bf16 v[72:75], v[148:151], v[220:223], v[72:75]
	v_mfma_f32_16x16x32_bf16 v[72:75], v[144:147], v[216:219], v[72:75]
	s_barrier
	s_mov_b32 m0, s49
	ds_read_b128 v[180:183], v163 offset:49152
	ds_read_b128 v[190:193], v163 offset:50176
	ds_read_b128 v[194:197], v163 offset:51200
	ds_read_b128 v[198:201], v163 offset:52224
	ds_read_b128 v[202:205], v163 offset:53248
	ds_read_b128 v[206:209], v163 offset:54272
	ds_read_b128 v[216:219], v163 offset:55296
	ds_read_b128 v[220:223], v163 offset:56320
	s_add_u32 s70, s56, s78
	s_addc_u32 s71, s57, s79
	global_load_lds_dwordx4 v132, s[70:71]
	s_mov_b32 m0, s50
	s_nop 0
	s_add_u32 s70, s56, s84
	s_addc_u32 s71, s57, s85
	global_load_lds_dwordx4 v132, s[70:71]
	s_mov_b32 m0, s51
	s_add_u32 s70, s56, s62
	s_addc_u32 s71, s57, s63
	global_load_lds_dwordx4 v132, s[70:71]
	s_mov_b32 m0, s52
	s_nop 0
	s_add_u32 s70, s56, s66
	s_addc_u32 s71, s57, s67
	global_load_lds_dwordx4 v132, s[70:71]
	s_mov_b32 m0, s0
	s_nop 0
	s_add_u32 s70, s54, s78
	s_addc_u32 s71, s55, s79
	global_load_lds_dwordx4 v134, s[70:71]
	s_mov_b32 m0, s41
	s_nop 0
	s_add_u32 s70, s54, s92
	s_addc_u32 s71, s55, s93
	global_load_lds_dwordx4 v134, s[70:71]
	s_waitcnt vmcnt(8)
	s_waitcnt lgkmcnt(0)
	s_barrier
	v_mfma_f32_16x16x32_bf16 v[56:59], v[144:147], v[180:183], v[56:59]
	v_mfma_f32_16x16x32_bf16 v[56:59], v[148:151], v[190:193], v[56:59]
	v_mfma_f32_16x16x32_bf16 v[52:55], v[156:159], v[190:193], v[52:55]
	v_mfma_f32_16x16x32_bf16 v[52:55], v[152:155], v[180:183], v[52:55]
	v_mfma_f32_16x16x32_bf16 v[64:67], v[164:167], v[180:183], v[64:67]
	v_mfma_f32_16x16x32_bf16 v[64:67], v[168:171], v[190:193], v[64:67]
	v_mfma_f32_16x16x32_bf16 v[60:63], v[176:179], v[190:193], v[60:63]
	v_mfma_f32_16x16x32_bf16 v[60:63], v[172:175], v[180:183], v[60:63]
	v_mfma_f32_16x16x32_bf16 v[44:47], v[172:175], v[194:197], v[44:47]
	v_mfma_f32_16x16x32_bf16 v[44:47], v[176:179], v[198:201], v[44:47]
	v_mfma_f32_16x16x32_bf16 v[48:51], v[168:171], v[198:201], v[48:51]
	v_mfma_f32_16x16x32_bf16 v[48:51], v[164:167], v[194:197], v[48:51]
	v_mfma_f32_16x16x32_bf16 v[36:39], v[152:155], v[194:197], v[36:39]
	v_mfma_f32_16x16x32_bf16 v[36:39], v[156:159], v[198:201], v[36:39]
	v_mfma_f32_16x16x32_bf16 v[40:43], v[148:151], v[198:201], v[40:43]
	v_mfma_f32_16x16x32_bf16 v[40:43], v[144:147], v[194:197], v[40:43]
	v_mfma_f32_16x16x32_bf16 v[24:27], v[144:147], v[202:205], v[24:27]
	v_mfma_f32_16x16x32_bf16 v[24:27], v[148:151], v[206:209], v[24:27]
	v_mfma_f32_16x16x32_bf16 v[20:23], v[156:159], v[206:209], v[20:23]
	v_mfma_f32_16x16x32_bf16 v[20:23], v[152:155], v[202:205], v[20:23]
	v_mfma_f32_16x16x32_bf16 v[32:35], v[164:167], v[202:205], v[32:35]
	v_mfma_f32_16x16x32_bf16 v[32:35], v[168:171], v[206:209], v[32:35]
	v_mfma_f32_16x16x32_bf16 v[28:31], v[176:179], v[206:209], v[28:31]
	v_mfma_f32_16x16x32_bf16 v[28:31], v[172:175], v[202:205], v[28:31]
	v_mfma_f32_16x16x32_bf16 v[12:15], v[172:175], v[216:219], v[12:15]
	v_mfma_f32_16x16x32_bf16 v[12:15], v[176:179], v[220:223], v[12:15]
	v_mfma_f32_16x16x32_bf16 v[16:19], v[168:171], v[220:223], v[16:19]
	v_mfma_f32_16x16x32_bf16 v[16:19], v[164:167], v[216:219], v[16:19]
	v_mfma_f32_16x16x32_bf16 v[4:7], v[152:155], v[216:219], v[4:7]
	v_mfma_f32_16x16x32_bf16 v[4:7], v[156:159], v[220:223], v[4:7]
	v_mfma_f32_16x16x32_bf16 v[8:11], v[148:151], v[220:223], v[8:11]
	v_mfma_f32_16x16x32_bf16 v[8:11], v[144:147], v[216:219], v[8:11]
	s_barrier
	s_add_i32 s30, s30, 2
	s_add_u32 s10, s10, 0x100
	s_addc_u32 s11, s11, 0
	s_add_u32 s28, s28, 0x100
	s_addc_u32 s29, s29, 0
	s_cmp_gt_u32 s30, 29
	s_cbranch_scc0 .LBB0_130
	s_and_b64 vcc, exec, s[20:21]
	s_cbranch_vccz .LBB0_133
	s_barrier

.LBB0_233:
	ds_read_b128 v[120:123], v116
	ds_read_b128 v[132:135], v116 offset:1024
	ds_read_b128 v[144:147], v116 offset:2048
	ds_read_b128 v[148:151], v116 offset:3072
	ds_read_b128 v[152:155], v117
	ds_read_b128 v[156:159], v117 offset:1024
	ds_read_b128 v[166:169], v117 offset:2048
	ds_read_b128 v[170:173], v117 offset:3072
	s_add_u32 s49, s26, 0xffea0080
	s_addc_u32 s50, s27, -1
	s_cmpk_eq_i32 s48, 0x54
	s_cselect_b32 s51, s21, s50
	s_cselect_b32 s50, s20, s49
	s_cselect_b32 s53, s23, s25
	s_cselect_b32 s52, s22, s24
	s_mov_b32 m0, s0
	ds_read_b128 v[180:183], v178
	ds_read_b128 v[184:187], v178 offset:1024
	ds_read_b128 v[190:193], v178 offset:2048
	ds_read_b128 v[194:197], v178 offset:3072
	ds_read_b128 v[198:201], v178 offset:4096
	ds_read_b128 v[202:205], v178 offset:5120
	ds_read_b128 v[206:209], v178 offset:6144
	ds_read_b128 v[216:219], v178 offset:7168
	global_load_lds_dwordx4 v164, s[26:27]
	s_mov_b32 m0, s4
	s_nop 0
	s_add_u32 s70, s26, s86
	s_addc_u32 s71, s27, s87
	global_load_lds_dwordx4 v164, s[70:71]
	s_waitcnt vmcnt(8)
	s_waitcnt lgkmcnt(0)
	s_barrier
	v_mfma_f32_16x16x32_bf16 v[140:143], v[120:123], v[180:183], v[140:143]
	v_mfma_f32_16x16x32_bf16 v[140:143], v[132:135], v[184:187], v[140:143]
	v_mfma_f32_16x16x32_bf16 v[136:139], v[148:151], v[184:187], v[136:139]
	v_mfma_f32_16x16x32_bf16 v[136:139], v[144:147], v[180:183], v[136:139]
	v_mfma_f32_16x16x32_bf16 v[128:131], v[152:155], v[180:183], v[128:131]
	v_mfma_f32_16x16x32_bf16 v[128:131], v[156:159], v[184:187], v[128:131]
	v_mfma_f32_16x16x32_bf16 v[124:127], v[170:173], v[184:187], v[124:127]
	v_mfma_f32_16x16x32_bf16 v[124:127], v[166:169], v[180:183], v[124:127]
	v_mfma_f32_16x16x32_bf16 v[100:103], v[166:169], v[190:193], v[100:103]
	v_mfma_f32_16x16x32_bf16 v[100:103], v[170:173], v[194:197], v[100:103]
	v_mfma_f32_16x16x32_bf16 v[104:107], v[156:159], v[194:197], v[104:107]
	v_mfma_f32_16x16x32_bf16 v[104:107], v[152:155], v[190:193], v[104:107]
	v_mfma_f32_16x16x32_bf16 v[108:111], v[144:147], v[190:193], v[108:111]
	v_mfma_f32_16x16x32_bf16 v[108:111], v[148:151], v[194:197], v[108:111]
	v_mfma_f32_16x16x32_bf16 v[112:115], v[132:135], v[194:197], v[112:115]
	v_mfma_f32_16x16x32_bf16 v[112:115], v[120:123], v[190:193], v[112:115]
	v_mfma_f32_16x16x32_bf16 v[96:99], v[120:123], v[198:201], v[96:99]
	v_mfma_f32_16x16x32_bf16 v[96:99], v[132:135], v[202:205], v[96:99]
	v_mfma_f32_16x16x32_bf16 v[92:95], v[148:151], v[202:205], v[92:95]
	v_mfma_f32_16x16x32_bf16 v[92:95], v[144:147], v[198:201], v[92:95]
	v_mfma_f32_16x16x32_bf16 v[88:91], v[152:155], v[198:201], v[88:91]
	v_mfma_f32_16x16x32_bf16 v[88:91], v[156:159], v[202:205], v[88:91]
	v_mfma_f32_16x16x32_bf16 v[84:87], v[170:173], v[202:205], v[84:87]
	v_mfma_f32_16x16x32_bf16 v[84:87], v[166:169], v[198:201], v[84:87]
	v_mfma_f32_16x16x32_bf16 v[68:71], v[166:169], v[206:209], v[68:71]
	v_mfma_f32_16x16x32_bf16 v[68:71], v[170:173], v[216:219], v[68:71]
	v_mfma_f32_16x16x32_bf16 v[72:75], v[156:159], v[216:219], v[72:75]
	v_mfma_f32_16x16x32_bf16 v[72:75], v[152:155], v[206:209], v[72:75]
	v_mfma_f32_16x16x32_bf16 v[76:79], v[144:147], v[206:209], v[76:79]
	v_mfma_f32_16x16x32_bf16 v[76:79], v[148:151], v[216:219], v[76:79]
	v_mfma_f32_16x16x32_bf16 v[80:83], v[132:135], v[216:219], v[80:83]
	v_mfma_f32_16x16x32_bf16 v[80:83], v[120:123], v[206:209], v[80:83]
	s_barrier
	s_mov_b32 m0, s5
	ds_read_b128 v[180:183], v178 offset:16384
	ds_read_b128 v[184:187], v178 offset:17408
	ds_read_b128 v[190:193], v178 offset:18432
	ds_read_b128 v[194:197], v178 offset:19456
	ds_read_b128 v[198:201], v178 offset:20480
	ds_read_b128 v[202:205], v178 offset:21504
	ds_read_b128 v[206:209], v178 offset:22528
	ds_read_b128 v[216:219], v178 offset:23552
	global_load_lds_dwordx4 v162, s[52:53]
	s_mov_b32 m0, s33
	s_nop 0
	s_add_u32 s70, s52, s86
	s_addc_u32 s71, s53, s87
	global_load_lds_dwordx4 v162, s[70:71]
	s_mov_b32 m0, s42
	s_nop 0
	s_add_u32 s70, s52, s54
	s_addc_u32 s71, s53, s55
	global_load_lds_dwordx4 v162, s[70:71]
	s_mov_b32 m0, s43
	s_nop 0
	s_add_u32 s70, s52, s56
	s_addc_u32 s71, s53, s57
	global_load_lds_dwordx4 v162, s[70:71]
	s_mov_b32 m0, s31
	s_nop 0
	global_load_lds_dwordx4 v160, s[50:51]
	s_mov_b32 m0, s34
	s_nop 0
	s_add_u32 s70, s50, s86
	s_addc_u32 s71, s51, s87
	global_load_lds_dwordx4 v160, s[70:71]
	s_waitcnt vmcnt(8)
	s_waitcnt lgkmcnt(0)
	s_barrier
	v_mfma_f32_16x16x32_bf16 v[56:59], v[120:123], v[180:183], v[56:59]
	v_mfma_f32_16x16x32_bf16 v[56:59], v[132:135], v[184:187], v[56:59]
	v_mfma_f32_16x16x32_bf16 v[52:55], v[148:151], v[184:187], v[52:55]
	v_mfma_f32_16x16x32_bf16 v[52:55], v[144:147], v[180:183], v[52:55]
	v_mfma_f32_16x16x32_bf16 v[64:67], v[152:155], v[180:183], v[64:67]
	v_mfma_f32_16x16x32_bf16 v[64:67], v[156:159], v[184:187], v[64:67]
	v_mfma_f32_16x16x32_bf16 v[60:63], v[170:173], v[184:187], v[60:63]
	v_mfma_f32_16x16x32_bf16 v[60:63], v[166:169], v[180:183], v[60:63]
	v_mfma_f32_16x16x32_bf16 v[36:39], v[166:169], v[190:193], v[36:39]
	v_mfma_f32_16x16x32_bf16 v[36:39], v[170:173], v[194:197], v[36:39]
	v_mfma_f32_16x16x32_bf16 v[40:43], v[156:159], v[194:197], v[40:43]
	v_mfma_f32_16x16x32_bf16 v[40:43], v[152:155], v[190:193], v[40:43]
	v_mfma_f32_16x16x32_bf16 v[44:47], v[144:147], v[190:193], v[44:47]
	v_mfma_f32_16x16x32_bf16 v[44:47], v[148:151], v[194:197], v[44:47]
	v_mfma_f32_16x16x32_bf16 v[48:51], v[132:135], v[194:197], v[48:51]
	v_mfma_f32_16x16x32_bf16 v[48:51], v[120:123], v[190:193], v[48:51]
	v_mfma_f32_16x16x32_bf16 v[32:35], v[120:123], v[198:201], v[32:35]
	v_mfma_f32_16x16x32_bf16 v[32:35], v[132:135], v[202:205], v[32:35]
	v_mfma_f32_16x16x32_bf16 v[28:31], v[148:151], v[202:205], v[28:31]
	v_mfma_f32_16x16x32_bf16 v[28:31], v[144:147], v[198:201], v[28:31]
	v_mfma_f32_16x16x32_bf16 v[24:27], v[152:155], v[198:201], v[24:27]
	v_mfma_f32_16x16x32_bf16 v[24:27], v[156:159], v[202:205], v[24:27]
	v_mfma_f32_16x16x32_bf16 v[20:23], v[170:173], v[202:205], v[20:23]
	v_mfma_f32_16x16x32_bf16 v[20:23], v[166:169], v[198:201], v[20:23]
	v_mfma_f32_16x16x32_bf16 v[4:7], v[166:169], v[206:209], v[4:7]
	v_mfma_f32_16x16x32_bf16 v[4:7], v[170:173], v[216:219], v[4:7]
	v_mfma_f32_16x16x32_bf16 v[8:11], v[156:159], v[216:219], v[8:11]
	v_mfma_f32_16x16x32_bf16 v[8:11], v[152:155], v[206:209], v[8:11]
	v_mfma_f32_16x16x32_bf16 v[12:15], v[144:147], v[206:209], v[12:15]
	v_mfma_f32_16x16x32_bf16 v[12:15], v[148:151], v[216:219], v[12:15]
	v_mfma_f32_16x16x32_bf16 v[16:19], v[132:135], v[216:219], v[16:19]
	v_mfma_f32_16x16x32_bf16 v[16:19], v[120:123], v[206:209], v[16:19]
	s_barrier
; #define PG8_MMA(ai, bj, At, Bt) do { __builtin_amdgcn_s_setprio(1); _Pragma("unroll") for (int m = 0; m < 4; ++m) _Pragma("unroll") for (int n = 0; n < 2; ++n) _Pragma("unroll") for (int k = 0; k < 2; ++k) \
;         acc[ai][bj][m][n] = __builtin_amdgcn_mfma_f32_16x16x32_bf16(Bt[n][k], At[m][k], acc[ai][bj][m][n], 0, 0, 0); __builtin_amdgcn_s_setprio(0); } while (0)
; #define PG8_WAIT_V(n) asm volatile("s_waitcnt vmcnt(" #n ")" ::: "memory")
; #define PG8_TRIP_HEAD(T) const int t = (T); const bool last = (t == nt - 2); \
;             const char* a1 = cA + (size_t)(t + 1) * kstep; \
;             const char* a2 = last ? nA : cA + (size_t)(t + 2) * kstep; const char* b2 = last ? nB : cB + (size_t)(t + 2) * kstep; \
;             const char* a3 = a2 + kstep; const char* b3 = b2 + kstep; \
;             if (last && has_next) S.a_ready(nxt);
; template <class Epi, class Sched, bool ALIGN_EPI = false, bool SP2 = false>
; __device__ __forceinline__ void gemm_phase(PG8_LAS unsigned char* lds, const Gemm g, const Sched& S, const Epi& E) {
;     ...
;         if constexpr (SP2) {
;             { PG8_TRIP_HEAD(0) PG8_TRIP_SP2(asm volatile("s_waitcnt vmcnt(%0)" :: "n"(8 + Epi::NST) : "memory"), PG8_MMAZ) }
;             for (int tt = 2; tt < nt; tt += 2) { PG8_TRIP_HEAD(tt) PG8_TRIP_SP2(PG8_WAIT_V(8), PG8_MMA) }
	ds_read_b128 v[120:123], v118
	ds_read_b128 v[132:135], v118 offset:1024
	ds_read_b128 v[144:147], v118 offset:2048
	ds_read_b128 v[148:151], v118 offset:3072
	ds_read_b128 v[152:155], v119
	ds_read_b128 v[156:159], v119 offset:1024
	ds_read_b128 v[166:169], v119 offset:2048
	ds_read_b128 v[170:173], v119 offset:3072
	s_mov_b32 m0, s35
	ds_read_b128 v[180:183], v178 offset:32768
	ds_read_b128 v[184:187], v178 offset:33792
	ds_read_b128 v[190:193], v178 offset:34816
	ds_read_b128 v[194:197], v178 offset:35840
	ds_read_b128 v[198:201], v178 offset:36864
	ds_read_b128 v[202:205], v178 offset:37888
	ds_read_b128 v[206:209], v178 offset:38912
	ds_read_b128 v[216:219], v178 offset:39936
	s_add_u32 s70, s50, s54
	s_addc_u32 s71, s51, s55
	global_load_lds_dwordx4 v160, s[70:71]
	s_mov_b32 m0, s36
	s_nop 0
	s_add_u32 s70, s50, s56
	s_addc_u32 s71, s51, s57
	global_load_lds_dwordx4 v160, s[70:71]
	s_waitcnt vmcnt(8)
	s_waitcnt lgkmcnt(0)
	s_barrier
	v_mfma_f32_16x16x32_bf16 v[140:143], v[120:123], v[180:183], v[140:143]
	v_mfma_f32_16x16x32_bf16 v[140:143], v[132:135], v[184:187], v[140:143]
	v_mfma_f32_16x16x32_bf16 v[136:139], v[148:151], v[184:187], v[136:139]
	v_mfma_f32_16x16x32_bf16 v[136:139], v[144:147], v[180:183], v[136:139]
	v_mfma_f32_16x16x32_bf16 v[128:131], v[152:155], v[180:183], v[128:131]
	v_mfma_f32_16x16x32_bf16 v[128:131], v[156:159], v[184:187], v[128:131]
	v_mfma_f32_16x16x32_bf16 v[124:127], v[170:173], v[184:187], v[124:127]
	v_mfma_f32_16x16x32_bf16 v[124:127], v[166:169], v[180:183], v[124:127]
	v_mfma_f32_16x16x32_bf16 v[100:103], v[166:169], v[190:193], v[100:103]
	v_mfma_f32_16x16x32_bf16 v[100:103], v[170:173], v[194:197], v[100:103]
	v_mfma_f32_16x16x32_bf16 v[104:107], v[156:159], v[194:197], v[104:107]
	v_mfma_f32_16x16x32_bf16 v[104:107], v[152:155], v[190:193], v[104:107]
	v_mfma_f32_16x16x32_bf16 v[108:111], v[144:147], v[190:193], v[108:111]
	v_mfma_f32_16x16x32_bf16 v[108:111], v[148:151], v[194:197], v[108:111]
	v_mfma_f32_16x16x32_bf16 v[112:115], v[132:135], v[194:197], v[112:115]
	v_mfma_f32_16x16x32_bf16 v[112:115], v[120:123], v[190:193], v[112:115]
	v_mfma_f32_16x16x32_bf16 v[96:99], v[120:123], v[198:201], v[96:99]
	v_mfma_f32_16x16x32_bf16 v[96:99], v[132:135], v[202:205], v[96:99]
	v_mfma_f32_16x16x32_bf16 v[92:95], v[148:151], v[202:205], v[92:95]
	v_mfma_f32_16x16x32_bf16 v[92:95], v[144:147], v[198:201], v[92:95]
	v_mfma_f32_16x16x32_bf16 v[88:91], v[152:155], v[198:201], v[88:91]
	v_mfma_f32_16x16x32_bf16 v[88:91], v[156:159], v[202:205], v[88:91]
	v_mfma_f32_16x16x32_bf16 v[84:87], v[170:173], v[202:205], v[84:87]
	v_mfma_f32_16x16x32_bf16 v[84:87], v[166:169], v[198:201], v[84:87]
	v_mfma_f32_16x16x32_bf16 v[68:71], v[166:169], v[206:209], v[68:71]
	v_mfma_f32_16x16x32_bf16 v[68:71], v[170:173], v[216:219], v[68:71]
	v_mfma_f32_16x16x32_bf16 v[72:75], v[156:159], v[216:219], v[72:75]
	v_mfma_f32_16x16x32_bf16 v[72:75], v[152:155], v[206:209], v[72:75]
	v_mfma_f32_16x16x32_bf16 v[76:79], v[144:147], v[206:209], v[76:79]
	v_mfma_f32_16x16x32_bf16 v[76:79], v[148:151], v[216:219], v[76:79]
	v_mfma_f32_16x16x32_bf16 v[80:83], v[132:135], v[216:219], v[80:83]
	v_mfma_f32_16x16x32_bf16 v[80:83], v[120:123], v[206:209], v[80:83]
	s_barrier
	s_mov_b32 m0, s44
	ds_read_b128 v[180:183], v178 offset:49152
	ds_read_b128 v[184:187], v178 offset:50176
	ds_read_b128 v[190:193], v178 offset:51200
	ds_read_b128 v[194:197], v178 offset:52224
	ds_read_b128 v[198:201], v178 offset:53248
	ds_read_b128 v[202:205], v178 offset:54272
	ds_read_b128 v[206:209], v178 offset:55296
	ds_read_b128 v[216:219], v178 offset:56320
	s_add_u32 s70, s52, s78
	s_addc_u32 s71, s53, s79
	global_load_lds_dwordx4 v162, s[70:71]
	s_mov_b32 m0, s45
	s_nop 0
	s_add_u32 s70, s52, s60
	s_addc_u32 s71, s53, s61
	global_load_lds_dwordx4 v162, s[70:71]
	s_mov_b32 m0, s46
	s_add_u32 s70, s52, s62
	s_addc_u32 s71, s53, s63
	global_load_lds_dwordx4 v162, s[70:71]
	s_mov_b32 m0, s47
	s_nop 0
	s_add_u32 s70, s52, s64
	s_addc_u32 s71, s53, s65
	global_load_lds_dwordx4 v162, s[70:71]
	s_mov_b32 m0, s37
	s_nop 0
	s_add_u32 s70, s50, s78
	s_addc_u32 s71, s51, s79
	global_load_lds_dwordx4 v160, s[70:71]
	s_mov_b32 m0, s38
	s_nop 0
	s_add_u32 s70, s50, s60
	s_addc_u32 s71, s51, s61
	global_load_lds_dwordx4 v160, s[70:71]
	s_waitcnt vmcnt(8)
	s_waitcnt lgkmcnt(0)
	s_barrier
	v_mfma_f32_16x16x32_bf16 v[56:59], v[120:123], v[180:183], v[56:59]
	v_mfma_f32_16x16x32_bf16 v[56:59], v[132:135], v[184:187], v[56:59]
	v_mfma_f32_16x16x32_bf16 v[52:55], v[148:151], v[184:187], v[52:55]
	v_mfma_f32_16x16x32_bf16 v[52:55], v[144:147], v[180:183], v[52:55]
	v_mfma_f32_16x16x32_bf16 v[64:67], v[152:155], v[180:183], v[64:67]
	v_mfma_f32_16x16x32_bf16 v[64:67], v[156:159], v[184:187], v[64:67]
	v_mfma_f32_16x16x32_bf16 v[60:63], v[170:173], v[184:187], v[60:63]
	v_mfma_f32_16x16x32_bf16 v[60:63], v[166:169], v[180:183], v[60:63]
	v_mfma_f32_16x16x32_bf16 v[36:39], v[166:169], v[190:193], v[36:39]
	v_mfma_f32_16x16x32_bf16 v[36:39], v[170:173], v[194:197], v[36:39]
	v_mfma_f32_16x16x32_bf16 v[40:43], v[156:159], v[194:197], v[40:43]
	v_mfma_f32_16x16x32_bf16 v[40:43], v[152:155], v[190:193], v[40:43]
	v_mfma_f32_16x16x32_bf16 v[44:47], v[144:147], v[190:193], v[44:47]
	v_mfma_f32_16x16x32_bf16 v[44:47], v[148:151], v[194:197], v[44:47]
	v_mfma_f32_16x16x32_bf16 v[48:51], v[132:135], v[194:197], v[48:51]
	v_mfma_f32_16x16x32_bf16 v[48:51], v[120:123], v[190:193], v[48:51]
	v_mfma_f32_16x16x32_bf16 v[32:35], v[120:123], v[198:201], v[32:35]
	v_mfma_f32_16x16x32_bf16 v[32:35], v[132:135], v[202:205], v[32:35]
	v_mfma_f32_16x16x32_bf16 v[28:31], v[148:151], v[202:205], v[28:31]
	v_mfma_f32_16x16x32_bf16 v[28:31], v[144:147], v[198:201], v[28:31]
	v_mfma_f32_16x16x32_bf16 v[24:27], v[152:155], v[198:201], v[24:27]
	v_mfma_f32_16x16x32_bf16 v[24:27], v[156:159], v[202:205], v[24:27]
	v_mfma_f32_16x16x32_bf16 v[20:23], v[170:173], v[202:205], v[20:23]
	v_mfma_f32_16x16x32_bf16 v[20:23], v[166:169], v[198:201], v[20:23]
	v_mfma_f32_16x16x32_bf16 v[4:7], v[166:169], v[206:209], v[4:7]
	v_mfma_f32_16x16x32_bf16 v[4:7], v[170:173], v[216:219], v[4:7]
	v_mfma_f32_16x16x32_bf16 v[8:11], v[156:159], v[216:219], v[8:11]
	v_mfma_f32_16x16x32_bf16 v[8:11], v[152:155], v[206:209], v[8:11]
	v_mfma_f32_16x16x32_bf16 v[12:15], v[144:147], v[206:209], v[12:15]
	v_mfma_f32_16x16x32_bf16 v[12:15], v[148:151], v[216:219], v[12:15]
	v_mfma_f32_16x16x32_bf16 v[16:19], v[132:135], v[216:219], v[16:19]
	v_mfma_f32_16x16x32_bf16 v[16:19], v[120:123], v[206:209], v[16:19]
	s_barrier
	s_add_i32 s48, s48, 2
	s_add_u32 s26, s26, 0x100
	s_addc_u32 s27, s27, 0
	s_add_u32 s24, s24, 0x100
	s_addc_u32 s25, s25, 0
	s_cmpk_gt_u32 s48, 0x55
	s_cbranch_scc0 .LBB0_233
	s_and_b64 vcc, exec, s[18:19]
	s_cbranch_vccz .LBB0_236
	s_barrier

.LBB0_324:
	ds_read_b128 v[136:139], v132
	ds_read_b128 v[140:143], v132 offset:1024
	ds_read_b128 v[144:147], v132 offset:2048
	ds_read_b128 v[148:151], v132 offset:3072
	ds_read_b128 v[152:155], v133
	ds_read_b128 v[156:159], v133 offset:1024
	ds_read_b128 v[160:163], v133 offset:2048
	ds_read_b128 v[174:177], v133 offset:3072
	s_add_u32 s15, s10, 0xfff7c080
	s_addc_u32 s50, s11, -1
	s_cmp_eq_u32 s14, 28
	s_cselect_b32 s51, s25, s50
	s_cselect_b32 s50, s24, s15
	s_cselect_b32 s53, s3, s13
	s_cselect_b32 s52, s4, s12
	s_mov_b32 m0, s5
	ds_read_b128 v[178:181], v200
	ds_read_b128 v[182:185], v200 offset:1024
	ds_read_b128 v[186:189], v200 offset:2048
	ds_read_b128 v[190:193], v200 offset:3072
	ds_read_b128 v[202:205], v200 offset:4096
	ds_read_b128 v[206:209], v200 offset:5120
	ds_read_b128 v[216:219], v200 offset:6144
	ds_read_b128 v[220:223], v200 offset:7168
	global_load_lds_dwordx4 v172, s[10:11]
	s_mov_b32 m0, s23
	s_nop 0
	s_add_u32 s70, s10, s96
	s_addc_u32 s71, s11, s97
	global_load_lds_dwordx4 v172, s[70:71]
	s_waitcnt vmcnt(8)
	s_waitcnt lgkmcnt(0)
	s_barrier
	v_mfma_f32_16x16x32_bf16 v[120:123], v[136:139], v[178:181], v[120:123]
	v_mfma_f32_16x16x32_bf16 v[120:123], v[140:143], v[182:185], v[120:123]
	v_mfma_f32_16x16x32_bf16 v[116:119], v[148:151], v[182:185], v[116:119]
	v_mfma_f32_16x16x32_bf16 v[116:119], v[144:147], v[178:181], v[116:119]
	v_mfma_f32_16x16x32_bf16 v[128:131], v[152:155], v[178:181], v[128:131]
	v_mfma_f32_16x16x32_bf16 v[128:131], v[156:159], v[182:185], v[128:131]
	v_mfma_f32_16x16x32_bf16 v[124:127], v[174:177], v[182:185], v[124:127]
	v_mfma_f32_16x16x32_bf16 v[124:127], v[160:163], v[178:181], v[124:127]
	v_mfma_f32_16x16x32_bf16 v[108:111], v[160:163], v[186:189], v[108:111]
	v_mfma_f32_16x16x32_bf16 v[108:111], v[174:177], v[190:193], v[108:111]
	v_mfma_f32_16x16x32_bf16 v[112:115], v[156:159], v[190:193], v[112:115]
	v_mfma_f32_16x16x32_bf16 v[112:115], v[152:155], v[186:189], v[112:115]
	v_mfma_f32_16x16x32_bf16 v[100:103], v[144:147], v[186:189], v[100:103]
	v_mfma_f32_16x16x32_bf16 v[100:103], v[148:151], v[190:193], v[100:103]
	v_mfma_f32_16x16x32_bf16 v[104:107], v[140:143], v[190:193], v[104:107]
	v_mfma_f32_16x16x32_bf16 v[104:107], v[136:139], v[186:189], v[104:107]
	v_mfma_f32_16x16x32_bf16 v[88:91], v[136:139], v[202:205], v[88:91]
	v_mfma_f32_16x16x32_bf16 v[88:91], v[140:143], v[206:209], v[88:91]
	v_mfma_f32_16x16x32_bf16 v[84:87], v[148:151], v[206:209], v[84:87]
	v_mfma_f32_16x16x32_bf16 v[84:87], v[144:147], v[202:205], v[84:87]
	v_mfma_f32_16x16x32_bf16 v[96:99], v[152:155], v[202:205], v[96:99]
	v_mfma_f32_16x16x32_bf16 v[96:99], v[156:159], v[206:209], v[96:99]
	v_mfma_f32_16x16x32_bf16 v[92:95], v[174:177], v[206:209], v[92:95]
	v_mfma_f32_16x16x32_bf16 v[92:95], v[160:163], v[202:205], v[92:95]
	v_mfma_f32_16x16x32_bf16 v[76:79], v[160:163], v[216:219], v[76:79]
	v_mfma_f32_16x16x32_bf16 v[76:79], v[174:177], v[220:223], v[76:79]
	v_mfma_f32_16x16x32_bf16 v[80:83], v[156:159], v[220:223], v[80:83]
	v_mfma_f32_16x16x32_bf16 v[80:83], v[152:155], v[216:219], v[80:83]
	v_mfma_f32_16x16x32_bf16 v[68:71], v[144:147], v[216:219], v[68:71]
	v_mfma_f32_16x16x32_bf16 v[68:71], v[148:151], v[220:223], v[68:71]
	v_mfma_f32_16x16x32_bf16 v[72:75], v[140:143], v[220:223], v[72:75]
	v_mfma_f32_16x16x32_bf16 v[72:75], v[136:139], v[216:219], v[72:75]
	s_barrier
	s_mov_b32 m0, s28
	ds_read_b128 v[178:181], v200 offset:16384
	ds_read_b128 v[182:185], v200 offset:17408
	ds_read_b128 v[186:189], v200 offset:18432
	ds_read_b128 v[190:193], v200 offset:19456
	ds_read_b128 v[202:205], v200 offset:20480
	ds_read_b128 v[206:209], v200 offset:21504
	ds_read_b128 v[216:219], v200 offset:22528
	ds_read_b128 v[220:223], v200 offset:23552
	global_load_lds_dwordx4 v164, s[52:53]
	s_mov_b32 m0, s29
	s_nop 0
	s_add_u32 s70, s52, s90
	s_addc_u32 s71, s53, s91
	global_load_lds_dwordx4 v164, s[70:71]
	s_mov_b32 m0, s33
	s_nop 0
	s_add_u32 s70, s52, s54
	s_addc_u32 s71, s53, s55
	global_load_lds_dwordx4 v164, s[70:71]
	s_mov_b32 m0, s45
	s_nop 0
	s_add_u32 s70, s52, s60
	s_addc_u32 s71, s53, s61
	global_load_lds_dwordx4 v164, s[70:71]
	s_mov_b32 m0, s30
	s_nop 0
	global_load_lds_dwordx4 v166, s[50:51]
	s_mov_b32 m0, s31
	s_nop 0
	s_add_u32 s70, s50, s96
	s_addc_u32 s71, s51, s97
	global_load_lds_dwordx4 v166, s[70:71]
	s_waitcnt vmcnt(8)
	s_waitcnt lgkmcnt(0)
	s_barrier
	v_mfma_f32_16x16x32_bf16 v[56:59], v[136:139], v[178:181], v[56:59]
	v_mfma_f32_16x16x32_bf16 v[56:59], v[140:143], v[182:185], v[56:59]
	v_mfma_f32_16x16x32_bf16 v[52:55], v[148:151], v[182:185], v[52:55]
	v_mfma_f32_16x16x32_bf16 v[52:55], v[144:147], v[178:181], v[52:55]
	v_mfma_f32_16x16x32_bf16 v[64:67], v[152:155], v[178:181], v[64:67]
	v_mfma_f32_16x16x32_bf16 v[64:67], v[156:159], v[182:185], v[64:67]
	v_mfma_f32_16x16x32_bf16 v[60:63], v[174:177], v[182:185], v[60:63]
	v_mfma_f32_16x16x32_bf16 v[60:63], v[160:163], v[178:181], v[60:63]
	v_mfma_f32_16x16x32_bf16 v[44:47], v[160:163], v[186:189], v[44:47]
	v_mfma_f32_16x16x32_bf16 v[44:47], v[174:177], v[190:193], v[44:47]
	v_mfma_f32_16x16x32_bf16 v[48:51], v[156:159], v[190:193], v[48:51]
	v_mfma_f32_16x16x32_bf16 v[48:51], v[152:155], v[186:189], v[48:51]
	v_mfma_f32_16x16x32_bf16 v[36:39], v[144:147], v[186:189], v[36:39]
	v_mfma_f32_16x16x32_bf16 v[36:39], v[148:151], v[190:193], v[36:39]
	v_mfma_f32_16x16x32_bf16 v[40:43], v[140:143], v[190:193], v[40:43]
	v_mfma_f32_16x16x32_bf16 v[40:43], v[136:139], v[186:189], v[40:43]
	v_mfma_f32_16x16x32_bf16 v[24:27], v[136:139], v[202:205], v[24:27]
	v_mfma_f32_16x16x32_bf16 v[24:27], v[140:143], v[206:209], v[24:27]
	v_mfma_f32_16x16x32_bf16 v[20:23], v[148:151], v[206:209], v[20:23]
	v_mfma_f32_16x16x32_bf16 v[20:23], v[144:147], v[202:205], v[20:23]
	v_mfma_f32_16x16x32_bf16 v[32:35], v[152:155], v[202:205], v[32:35]
	v_mfma_f32_16x16x32_bf16 v[32:35], v[156:159], v[206:209], v[32:35]
	v_mfma_f32_16x16x32_bf16 v[28:31], v[174:177], v[206:209], v[28:31]
	v_mfma_f32_16x16x32_bf16 v[28:31], v[160:163], v[202:205], v[28:31]
	v_mfma_f32_16x16x32_bf16 v[12:15], v[160:163], v[216:219], v[12:15]
	v_mfma_f32_16x16x32_bf16 v[12:15], v[174:177], v[220:223], v[12:15]
	v_mfma_f32_16x16x32_bf16 v[16:19], v[156:159], v[220:223], v[16:19]
	v_mfma_f32_16x16x32_bf16 v[16:19], v[152:155], v[216:219], v[16:19]
	v_mfma_f32_16x16x32_bf16 v[4:7], v[144:147], v[216:219], v[4:7]
	v_mfma_f32_16x16x32_bf16 v[4:7], v[148:151], v[220:223], v[4:7]
	v_mfma_f32_16x16x32_bf16 v[8:11], v[140:143], v[220:223], v[8:11]
	v_mfma_f32_16x16x32_bf16 v[8:11], v[136:139], v[216:219], v[8:11]
	s_barrier
; #define PG8_MMA(ai, bj, At, Bt) do { __builtin_amdgcn_s_setprio(1); _Pragma("unroll") for (int m = 0; m < 4; ++m) _Pragma("unroll") for (int n = 0; n < 2; ++n) _Pragma("unroll") for (int k = 0; k < 2; ++k) \
;         acc[ai][bj][m][n] = __builtin_amdgcn_mfma_f32_16x16x32_bf16(Bt[n][k], At[m][k], acc[ai][bj][m][n], 0, 0, 0); __builtin_amdgcn_s_setprio(0); } while (0)
; #define PG8_WAIT_V(n) asm volatile("s_waitcnt vmcnt(" #n ")" ::: "memory")
; #define PG8_TRIP_HEAD(T) const int t = (T); const bool last = (t == nt - 2); \
;             const char* a1 = cA + (size_t)(t + 1) * kstep; \
;             const char* a2 = last ? nA : cA + (size_t)(t + 2) * kstep; const char* b2 = last ? nB : cB + (size_t)(t + 2) * kstep; \
;             const char* a3 = a2 + kstep; const char* b3 = b2 + kstep; \
;             if (last && has_next) S.a_ready(nxt);
; template <class Epi, class Sched, bool ALIGN_EPI = false, bool SP2 = false>
; __device__ __forceinline__ void gemm_phase(PG8_LAS unsigned char* lds, const Gemm g, const Sched& S, const Epi& E) {
;     ...
;         if constexpr (SP2) {
;             { PG8_TRIP_HEAD(0) PG8_TRIP_SP2(asm volatile("s_waitcnt vmcnt(%0)" :: "n"(8 + Epi::NST) : "memory"), PG8_MMAZ) }
;             for (int tt = 2; tt < nt; tt += 2) { PG8_TRIP_HEAD(tt) PG8_TRIP_SP2(PG8_WAIT_V(8), PG8_MMA) }
	ds_read_b128 v[136:139], v134
	ds_read_b128 v[140:143], v134 offset:1024
	ds_read_b128 v[144:147], v134 offset:2048
	ds_read_b128 v[148:151], v134 offset:3072
	ds_read_b128 v[152:155], v135
	ds_read_b128 v[156:159], v135 offset:1024
	ds_read_b128 v[160:163], v135 offset:2048
	ds_read_b128 v[174:177], v135 offset:3072
	s_mov_b32 m0, s34
	ds_read_b128 v[178:181], v200 offset:32768
	ds_read_b128 v[182:185], v200 offset:33792
	ds_read_b128 v[186:189], v200 offset:34816
	ds_read_b128 v[190:193], v200 offset:35840
	ds_read_b128 v[202:205], v200 offset:36864
	ds_read_b128 v[206:209], v200 offset:37888
	ds_read_b128 v[216:219], v200 offset:38912
	ds_read_b128 v[220:223], v200 offset:39936
	s_add_u32 s70, s50, s82
	s_addc_u32 s71, s51, s83
	global_load_lds_dwordx4 v166, s[70:71]
	s_mov_b32 m0, s35
	s_nop 0
	s_add_u32 s70, s50, s64
	s_addc_u32 s71, s51, s65
	global_load_lds_dwordx4 v166, s[70:71]
	s_waitcnt vmcnt(8)
	s_waitcnt lgkmcnt(0)
	s_barrier
	v_mfma_f32_16x16x32_bf16 v[120:123], v[136:139], v[178:181], v[120:123]
	v_mfma_f32_16x16x32_bf16 v[120:123], v[140:143], v[182:185], v[120:123]
	v_mfma_f32_16x16x32_bf16 v[116:119], v[148:151], v[182:185], v[116:119]
	v_mfma_f32_16x16x32_bf16 v[116:119], v[144:147], v[178:181], v[116:119]
	v_mfma_f32_16x16x32_bf16 v[128:131], v[152:155], v[178:181], v[128:131]
	v_mfma_f32_16x16x32_bf16 v[128:131], v[156:159], v[182:185], v[128:131]
	v_mfma_f32_16x16x32_bf16 v[124:127], v[174:177], v[182:185], v[124:127]
	v_mfma_f32_16x16x32_bf16 v[124:127], v[160:163], v[178:181], v[124:127]
	v_mfma_f32_16x16x32_bf16 v[108:111], v[160:163], v[186:189], v[108:111]
	v_mfma_f32_16x16x32_bf16 v[108:111], v[174:177], v[190:193], v[108:111]
	v_mfma_f32_16x16x32_bf16 v[112:115], v[156:159], v[190:193], v[112:115]
	v_mfma_f32_16x16x32_bf16 v[112:115], v[152:155], v[186:189], v[112:115]
	v_mfma_f32_16x16x32_bf16 v[100:103], v[144:147], v[186:189], v[100:103]
	v_mfma_f32_16x16x32_bf16 v[100:103], v[148:151], v[190:193], v[100:103]
	v_mfma_f32_16x16x32_bf16 v[104:107], v[140:143], v[190:193], v[104:107]
	v_mfma_f32_16x16x32_bf16 v[104:107], v[136:139], v[186:189], v[104:107]
	v_mfma_f32_16x16x32_bf16 v[88:91], v[136:139], v[202:205], v[88:91]
	v_mfma_f32_16x16x32_bf16 v[88:91], v[140:143], v[206:209], v[88:91]
	v_mfma_f32_16x16x32_bf16 v[84:87], v[148:151], v[206:209], v[84:87]
	v_mfma_f32_16x16x32_bf16 v[84:87], v[144:147], v[202:205], v[84:87]
	v_mfma_f32_16x16x32_bf16 v[96:99], v[152:155], v[202:205], v[96:99]
	v_mfma_f32_16x16x32_bf16 v[96:99], v[156:159], v[206:209], v[96:99]
	v_mfma_f32_16x16x32_bf16 v[92:95], v[174:177], v[206:209], v[92:95]
	v_mfma_f32_16x16x32_bf16 v[92:95], v[160:163], v[202:205], v[92:95]
	v_mfma_f32_16x16x32_bf16 v[76:79], v[160:163], v[216:219], v[76:79]
	v_mfma_f32_16x16x32_bf16 v[76:79], v[174:177], v[220:223], v[76:79]
	v_mfma_f32_16x16x32_bf16 v[80:83], v[156:159], v[220:223], v[80:83]
	v_mfma_f32_16x16x32_bf16 v[80:83], v[152:155], v[216:219], v[80:83]
	v_mfma_f32_16x16x32_bf16 v[68:71], v[144:147], v[216:219], v[68:71]
	v_mfma_f32_16x16x32_bf16 v[68:71], v[148:151], v[220:223], v[68:71]
	v_mfma_f32_16x16x32_bf16 v[72:75], v[140:143], v[220:223], v[72:75]
	v_mfma_f32_16x16x32_bf16 v[72:75], v[136:139], v[216:219], v[72:75]
	s_barrier
	s_mov_b32 m0, s46
	ds_read_b128 v[178:181], v200 offset:49152
	ds_read_b128 v[182:185], v200 offset:50176
	ds_read_b128 v[186:189], v200 offset:51200
	ds_read_b128 v[190:193], v200 offset:52224
	ds_read_b128 v[202:205], v200 offset:53248
	ds_read_b128 v[206:209], v200 offset:54272
	ds_read_b128 v[216:219], v200 offset:55296
	ds_read_b128 v[220:223], v200 offset:56320
	s_add_u32 s70, s52, s78
	s_addc_u32 s71, s53, s79
	global_load_lds_dwordx4 v164, s[70:71]
	s_mov_b32 m0, s47
	s_nop 0
	s_add_u32 s70, s52, s84
	s_addc_u32 s71, s53, s85
	global_load_lds_dwordx4 v164, s[70:71]
	s_mov_b32 m0, s48
	s_add_u32 s70, s52, s56
	s_addc_u32 s71, s53, s57
	global_load_lds_dwordx4 v164, s[70:71]
	s_mov_b32 m0, s49
	s_nop 0
	s_add_u32 s70, s52, s62
	s_addc_u32 s71, s53, s63
	global_load_lds_dwordx4 v164, s[70:71]
	s_mov_b32 m0, s38
	s_nop 0
	s_add_u32 s70, s50, s78
	s_addc_u32 s71, s51, s79
	global_load_lds_dwordx4 v166, s[70:71]
	s_mov_b32 m0, s39
	s_nop 0
	s_add_u32 s70, s50, s92
	s_addc_u32 s71, s51, s93
	global_load_lds_dwordx4 v166, s[70:71]
	s_waitcnt vmcnt(8)
	s_waitcnt lgkmcnt(0)
	s_barrier
	v_mfma_f32_16x16x32_bf16 v[56:59], v[136:139], v[178:181], v[56:59]
	v_mfma_f32_16x16x32_bf16 v[56:59], v[140:143], v[182:185], v[56:59]
	v_mfma_f32_16x16x32_bf16 v[52:55], v[148:151], v[182:185], v[52:55]
	v_mfma_f32_16x16x32_bf16 v[52:55], v[144:147], v[178:181], v[52:55]
	v_mfma_f32_16x16x32_bf16 v[64:67], v[152:155], v[178:181], v[64:67]
	v_mfma_f32_16x16x32_bf16 v[64:67], v[156:159], v[182:185], v[64:67]
	v_mfma_f32_16x16x32_bf16 v[60:63], v[174:177], v[182:185], v[60:63]
	v_mfma_f32_16x16x32_bf16 v[60:63], v[160:163], v[178:181], v[60:63]
	v_mfma_f32_16x16x32_bf16 v[44:47], v[160:163], v[186:189], v[44:47]
	v_mfma_f32_16x16x32_bf16 v[44:47], v[174:177], v[190:193], v[44:47]
	v_mfma_f32_16x16x32_bf16 v[48:51], v[156:159], v[190:193], v[48:51]
	v_mfma_f32_16x16x32_bf16 v[48:51], v[152:155], v[186:189], v[48:51]
	v_mfma_f32_16x16x32_bf16 v[36:39], v[144:147], v[186:189], v[36:39]
	v_mfma_f32_16x16x32_bf16 v[36:39], v[148:151], v[190:193], v[36:39]
	v_mfma_f32_16x16x32_bf16 v[40:43], v[140:143], v[190:193], v[40:43]
	v_mfma_f32_16x16x32_bf16 v[40:43], v[136:139], v[186:189], v[40:43]
	v_mfma_f32_16x16x32_bf16 v[24:27], v[136:139], v[202:205], v[24:27]
	v_mfma_f32_16x16x32_bf16 v[24:27], v[140:143], v[206:209], v[24:27]
	v_mfma_f32_16x16x32_bf16 v[20:23], v[148:151], v[206:209], v[20:23]
	v_mfma_f32_16x16x32_bf16 v[20:23], v[144:147], v[202:205], v[20:23]
	v_mfma_f32_16x16x32_bf16 v[32:35], v[152:155], v[202:205], v[32:35]
	v_mfma_f32_16x16x32_bf16 v[32:35], v[156:159], v[206:209], v[32:35]
	v_mfma_f32_16x16x32_bf16 v[28:31], v[174:177], v[206:209], v[28:31]
	v_mfma_f32_16x16x32_bf16 v[28:31], v[160:163], v[202:205], v[28:31]
	v_mfma_f32_16x16x32_bf16 v[12:15], v[160:163], v[216:219], v[12:15]
	v_mfma_f32_16x16x32_bf16 v[12:15], v[174:177], v[220:223], v[12:15]
	v_mfma_f32_16x16x32_bf16 v[16:19], v[156:159], v[220:223], v[16:19]
	v_mfma_f32_16x16x32_bf16 v[16:19], v[152:155], v[216:219], v[16:19]
	v_mfma_f32_16x16x32_bf16 v[4:7], v[144:147], v[216:219], v[4:7]
	v_mfma_f32_16x16x32_bf16 v[4:7], v[148:151], v[220:223], v[4:7]
	v_mfma_f32_16x16x32_bf16 v[8:11], v[140:143], v[220:223], v[8:11]
	v_mfma_f32_16x16x32_bf16 v[8:11], v[136:139], v[216:219], v[8:11]
	s_barrier
	s_add_i32 s14, s14, 2
	s_add_u32 s10, s10, 0x100
	s_addc_u32 s11, s11, 0
	s_add_u32 s12, s12, 0x100
	s_addc_u32 s13, s13, 0
	s_cmp_gt_u32 s14, 29
	s_cbranch_scc0 .LBB0_324
	s_and_b64 vcc, exec, s[18:19]
	s_cbranch_vccz .LBB0_327
	s_barrier

.LBB0_594:
	ds_read_b128 v[136:139], v116
	ds_read_b128 v[140:143], v116 offset:1024
	ds_read_b128 v[144:147], v116 offset:2048
	ds_read_b128 v[148:151], v116 offset:3072
	ds_read_b128 v[152:155], v117
	ds_read_b128 v[156:159], v117 offset:1024
	ds_read_b128 v[160:163], v117 offset:2048
	ds_read_b128 v[164:167], v117 offset:3072
	s_add_u32 s43, s20, 0xfff7c080
	s_addc_u32 s44, s21, -1
	s_cmp_eq_u32 s15, 28
	s_cselect_b32 s45, s17, s44
	s_cselect_b32 s44, s16, s43
	s_cselect_b32 s47, s4, s9
	s_cselect_b32 s46, s5, s8
	s_mov_b32 m0, s33
	ds_read_b128 v[168:171], v221
	ds_read_b128 v[172:175], v221 offset:1024
	ds_read_b128 v[176:179], v221 offset:2048
	ds_read_b128 v[180:183], v221 offset:3072
	ds_read_b128 v[184:187], v221 offset:4096
	ds_read_b128 v[188:191], v221 offset:5120
	ds_read_b128 v[202:205], v221 offset:6144
	ds_read_b128 v[206:209], v221 offset:7168
	global_load_lds_dwordx4 v200, s[20:21]
	s_mov_b32 m0, s34
	s_nop 0
	s_add_u32 s70, s20, s96
	s_addc_u32 s71, s21, s97
	global_load_lds_dwordx4 v200, s[70:71]
	s_waitcnt vmcnt(8)
	s_waitcnt lgkmcnt(0)
	s_barrier
	v_mfma_f32_16x16x32_bf16 v[130:133], v[136:139], v[168:171], v[130:133]
	v_mfma_f32_16x16x32_bf16 v[130:133], v[140:143], v[172:175], v[130:133]
	v_mfma_f32_16x16x32_bf16 v[126:129], v[148:151], v[172:175], v[126:129]
	v_mfma_f32_16x16x32_bf16 v[126:129], v[144:147], v[168:171], v[126:129]
	v_mfma_f32_16x16x32_bf16 v[122:125], v[152:155], v[168:171], v[122:125]
	v_mfma_f32_16x16x32_bf16 v[122:125], v[156:159], v[172:175], v[122:125]
	v_mfma_f32_16x16x32_bf16 v[118:121], v[164:167], v[172:175], v[118:121]
	v_mfma_f32_16x16x32_bf16 v[118:121], v[160:163], v[168:171], v[118:121]
	v_mfma_f32_16x16x32_bf16 v[100:103], v[160:163], v[176:179], v[100:103]
	v_mfma_f32_16x16x32_bf16 v[100:103], v[164:167], v[180:183], v[100:103]
	v_mfma_f32_16x16x32_bf16 v[104:107], v[156:159], v[180:183], v[104:107]
	v_mfma_f32_16x16x32_bf16 v[104:107], v[152:155], v[176:179], v[104:107]
	v_mfma_f32_16x16x32_bf16 v[108:111], v[144:147], v[176:179], v[108:111]
	v_mfma_f32_16x16x32_bf16 v[108:111], v[148:151], v[180:183], v[108:111]
	v_mfma_f32_16x16x32_bf16 v[112:115], v[140:143], v[180:183], v[112:115]
	v_mfma_f32_16x16x32_bf16 v[112:115], v[136:139], v[176:179], v[112:115]
	v_mfma_f32_16x16x32_bf16 v[96:99], v[136:139], v[184:187], v[96:99]
	v_mfma_f32_16x16x32_bf16 v[96:99], v[140:143], v[188:191], v[96:99]
	v_mfma_f32_16x16x32_bf16 v[92:95], v[148:151], v[188:191], v[92:95]
	v_mfma_f32_16x16x32_bf16 v[92:95], v[144:147], v[184:187], v[92:95]
	v_mfma_f32_16x16x32_bf16 v[88:91], v[152:155], v[184:187], v[88:91]
	v_mfma_f32_16x16x32_bf16 v[88:91], v[156:159], v[188:191], v[88:91]
	v_mfma_f32_16x16x32_bf16 v[84:87], v[164:167], v[188:191], v[84:87]
	v_mfma_f32_16x16x32_bf16 v[84:87], v[160:163], v[184:187], v[84:87]
	v_mfma_f32_16x16x32_bf16 v[68:71], v[160:163], v[202:205], v[68:71]
	v_mfma_f32_16x16x32_bf16 v[68:71], v[164:167], v[206:209], v[68:71]
	v_mfma_f32_16x16x32_bf16 v[72:75], v[156:159], v[206:209], v[72:75]
	v_mfma_f32_16x16x32_bf16 v[72:75], v[152:155], v[202:205], v[72:75]
	v_mfma_f32_16x16x32_bf16 v[76:79], v[144:147], v[202:205], v[76:79]
	v_mfma_f32_16x16x32_bf16 v[76:79], v[148:151], v[206:209], v[76:79]
	v_mfma_f32_16x16x32_bf16 v[80:83], v[140:143], v[206:209], v[80:83]
	v_mfma_f32_16x16x32_bf16 v[80:83], v[136:139], v[202:205], v[80:83]
	s_barrier
	s_mov_b32 m0, s35
	ds_read_b128 v[168:171], v221 offset:16384
	ds_read_b128 v[172:175], v221 offset:17408
	ds_read_b128 v[176:179], v221 offset:18432
	ds_read_b128 v[180:183], v221 offset:19456
	ds_read_b128 v[184:187], v221 offset:20480
	ds_read_b128 v[188:191], v221 offset:21504
	ds_read_b128 v[202:205], v221 offset:22528
	ds_read_b128 v[206:209], v221 offset:23552
	global_load_lds_dwordx4 v194, s[46:47]
	s_mov_b32 m0, s36
	s_nop 0
	s_add_u32 s70, s46, s90
	s_addc_u32 s71, s47, s91
	global_load_lds_dwordx4 v194, s[70:71]
	s_mov_b32 m0, s37
	s_nop 0
	s_add_u32 s70, s46, s48
	s_addc_u32 s71, s47, s49
	global_load_lds_dwordx4 v194, s[70:71]
	s_mov_b32 m0, s38
	s_nop 0
	s_add_u32 s70, s46, s52
	s_addc_u32 s71, s47, s53
	global_load_lds_dwordx4 v194, s[70:71]
	s_mov_b32 m0, s23
	s_nop 0
	global_load_lds_dwordx4 v196, s[44:45]
	s_mov_b32 m0, s24
	s_nop 0
	s_add_u32 s70, s44, s96
	s_addc_u32 s71, s45, s97
	global_load_lds_dwordx4 v196, s[70:71]
	s_waitcnt vmcnt(8)
	s_waitcnt lgkmcnt(0)
	s_barrier
	v_mfma_f32_16x16x32_bf16 v[64:67], v[136:139], v[168:171], v[64:67]
	v_mfma_f32_16x16x32_bf16 v[64:67], v[140:143], v[172:175], v[64:67]
	v_mfma_f32_16x16x32_bf16 v[60:63], v[148:151], v[172:175], v[60:63]
	v_mfma_f32_16x16x32_bf16 v[60:63], v[144:147], v[168:171], v[60:63]
	v_mfma_f32_16x16x32_bf16 v[56:59], v[152:155], v[168:171], v[56:59]
	v_mfma_f32_16x16x32_bf16 v[56:59], v[156:159], v[172:175], v[56:59]
	v_mfma_f32_16x16x32_bf16 v[52:55], v[164:167], v[172:175], v[52:55]
	v_mfma_f32_16x16x32_bf16 v[52:55], v[160:163], v[168:171], v[52:55]
	v_mfma_f32_16x16x32_bf16 v[36:39], v[160:163], v[176:179], v[36:39]
	v_mfma_f32_16x16x32_bf16 v[36:39], v[164:167], v[180:183], v[36:39]
	v_mfma_f32_16x16x32_bf16 v[40:43], v[156:159], v[180:183], v[40:43]
	v_mfma_f32_16x16x32_bf16 v[40:43], v[152:155], v[176:179], v[40:43]
	v_mfma_f32_16x16x32_bf16 v[44:47], v[144:147], v[176:179], v[44:47]
	v_mfma_f32_16x16x32_bf16 v[44:47], v[148:151], v[180:183], v[44:47]
	v_mfma_f32_16x16x32_bf16 v[48:51], v[140:143], v[180:183], v[48:51]
	v_mfma_f32_16x16x32_bf16 v[48:51], v[136:139], v[176:179], v[48:51]
	v_mfma_f32_16x16x32_bf16 v[32:35], v[136:139], v[184:187], v[32:35]
	v_mfma_f32_16x16x32_bf16 v[32:35], v[140:143], v[188:191], v[32:35]
	v_mfma_f32_16x16x32_bf16 v[28:31], v[148:151], v[188:191], v[28:31]
	v_mfma_f32_16x16x32_bf16 v[28:31], v[144:147], v[184:187], v[28:31]
	v_mfma_f32_16x16x32_bf16 v[24:27], v[152:155], v[184:187], v[24:27]
	v_mfma_f32_16x16x32_bf16 v[24:27], v[156:159], v[188:191], v[24:27]
	v_mfma_f32_16x16x32_bf16 v[20:23], v[164:167], v[188:191], v[20:23]
	v_mfma_f32_16x16x32_bf16 v[20:23], v[160:163], v[184:187], v[20:23]
	v_mfma_f32_16x16x32_bf16 v[4:7], v[160:163], v[202:205], v[4:7]
	v_mfma_f32_16x16x32_bf16 v[4:7], v[164:167], v[206:209], v[4:7]
	v_mfma_f32_16x16x32_bf16 v[8:11], v[156:159], v[206:209], v[8:11]
	v_mfma_f32_16x16x32_bf16 v[8:11], v[152:155], v[202:205], v[8:11]
	v_mfma_f32_16x16x32_bf16 v[12:15], v[144:147], v[202:205], v[12:15]
	v_mfma_f32_16x16x32_bf16 v[12:15], v[148:151], v[206:209], v[12:15]
	v_mfma_f32_16x16x32_bf16 v[16:19], v[140:143], v[206:209], v[16:19]
	v_mfma_f32_16x16x32_bf16 v[16:19], v[136:139], v[202:205], v[16:19]
	s_barrier
; #define PG8_MMA(ai, bj, At, Bt) do { __builtin_amdgcn_s_setprio(1); _Pragma("unroll") for (int m = 0; m < 4; ++m) _Pragma("unroll") for (int n = 0; n < 2; ++n) _Pragma("unroll") for (int k = 0; k < 2; ++k) \
;         acc[ai][bj][m][n] = __builtin_amdgcn_mfma_f32_16x16x32_bf16(Bt[n][k], At[m][k], acc[ai][bj][m][n], 0, 0, 0); __builtin_amdgcn_s_setprio(0); } while (0)
; #define PG8_WAIT_V(n) asm volatile("s_waitcnt vmcnt(" #n ")" ::: "memory")
; #define PG8_TRIP_HEAD(T) const int t = (T); const bool last = (t == nt - 2); \
;             const char* a1 = cA + (size_t)(t + 1) * kstep; \
;             const char* a2 = last ? nA : cA + (size_t)(t + 2) * kstep; const char* b2 = last ? nB : cB + (size_t)(t + 2) * kstep; \
;             const char* a3 = a2 + kstep; const char* b3 = b2 + kstep; \
;             if (last && has_next) S.a_ready(nxt);
; template <class Epi, class Sched, bool ALIGN_EPI = false, bool SP2 = false>
; __device__ __forceinline__ void gemm_phase(PG8_LAS unsigned char* lds, const Gemm g, const Sched& S, const Epi& E) {
;     ...
;         if constexpr (SP2) {
;             { PG8_TRIP_HEAD(0) PG8_TRIP_SP2(asm volatile("s_waitcnt vmcnt(%0)" :: "n"(8 + Epi::NST) : "memory"), PG8_MMAZ) }
;             for (int tt = 2; tt < nt; tt += 2) { PG8_TRIP_HEAD(tt) PG8_TRIP_SP2(PG8_WAIT_V(8), PG8_MMA) }
	ds_read_b128 v[136:139], v134
	ds_read_b128 v[140:143], v134 offset:1024
	ds_read_b128 v[144:147], v134 offset:2048
	ds_read_b128 v[148:151], v134 offset:3072
	ds_read_b128 v[152:155], v135
	ds_read_b128 v[156:159], v135 offset:1024
	ds_read_b128 v[160:163], v135 offset:2048
	ds_read_b128 v[164:167], v135 offset:3072
	s_mov_b32 m0, s25
	ds_read_b128 v[168:171], v221 offset:32768
	ds_read_b128 v[172:175], v221 offset:33792
	ds_read_b128 v[176:179], v221 offset:34816
	ds_read_b128 v[180:183], v221 offset:35840
	ds_read_b128 v[184:187], v221 offset:36864
	ds_read_b128 v[188:191], v221 offset:37888
	ds_read_b128 v[202:205], v221 offset:38912
	ds_read_b128 v[206:209], v221 offset:39936
	s_add_u32 s70, s44, s82
	s_addc_u32 s71, s45, s83
	global_load_lds_dwordx4 v196, s[70:71]
	s_mov_b32 m0, s26
	s_nop 0
	s_add_u32 s70, s44, s56
	s_addc_u32 s71, s45, s57
	global_load_lds_dwordx4 v196, s[70:71]
	s_waitcnt vmcnt(8)
	s_waitcnt lgkmcnt(0)
	s_barrier
	v_mfma_f32_16x16x32_bf16 v[130:133], v[136:139], v[168:171], v[130:133]
	v_mfma_f32_16x16x32_bf16 v[130:133], v[140:143], v[172:175], v[130:133]
	v_mfma_f32_16x16x32_bf16 v[126:129], v[148:151], v[172:175], v[126:129]
	v_mfma_f32_16x16x32_bf16 v[126:129], v[144:147], v[168:171], v[126:129]
	v_mfma_f32_16x16x32_bf16 v[122:125], v[152:155], v[168:171], v[122:125]
	v_mfma_f32_16x16x32_bf16 v[122:125], v[156:159], v[172:175], v[122:125]
	v_mfma_f32_16x16x32_bf16 v[118:121], v[164:167], v[172:175], v[118:121]
	v_mfma_f32_16x16x32_bf16 v[118:121], v[160:163], v[168:171], v[118:121]
	v_mfma_f32_16x16x32_bf16 v[100:103], v[160:163], v[176:179], v[100:103]
	v_mfma_f32_16x16x32_bf16 v[100:103], v[164:167], v[180:183], v[100:103]
	v_mfma_f32_16x16x32_bf16 v[104:107], v[156:159], v[180:183], v[104:107]
	v_mfma_f32_16x16x32_bf16 v[104:107], v[152:155], v[176:179], v[104:107]
	v_mfma_f32_16x16x32_bf16 v[108:111], v[144:147], v[176:179], v[108:111]
	v_mfma_f32_16x16x32_bf16 v[108:111], v[148:151], v[180:183], v[108:111]
	v_mfma_f32_16x16x32_bf16 v[112:115], v[140:143], v[180:183], v[112:115]
	v_mfma_f32_16x16x32_bf16 v[112:115], v[136:139], v[176:179], v[112:115]
	v_mfma_f32_16x16x32_bf16 v[96:99], v[136:139], v[184:187], v[96:99]
	v_mfma_f32_16x16x32_bf16 v[96:99], v[140:143], v[188:191], v[96:99]
	v_mfma_f32_16x16x32_bf16 v[92:95], v[148:151], v[188:191], v[92:95]
	v_mfma_f32_16x16x32_bf16 v[92:95], v[144:147], v[184:187], v[92:95]
	v_mfma_f32_16x16x32_bf16 v[88:91], v[152:155], v[184:187], v[88:91]
	v_mfma_f32_16x16x32_bf16 v[88:91], v[156:159], v[188:191], v[88:91]
	v_mfma_f32_16x16x32_bf16 v[84:87], v[164:167], v[188:191], v[84:87]
	v_mfma_f32_16x16x32_bf16 v[84:87], v[160:163], v[184:187], v[84:87]
	v_mfma_f32_16x16x32_bf16 v[68:71], v[160:163], v[202:205], v[68:71]
	v_mfma_f32_16x16x32_bf16 v[68:71], v[164:167], v[206:209], v[68:71]
	v_mfma_f32_16x16x32_bf16 v[72:75], v[156:159], v[206:209], v[72:75]
	v_mfma_f32_16x16x32_bf16 v[72:75], v[152:155], v[202:205], v[72:75]
	v_mfma_f32_16x16x32_bf16 v[76:79], v[144:147], v[202:205], v[76:79]
	v_mfma_f32_16x16x32_bf16 v[76:79], v[148:151], v[206:209], v[76:79]
	v_mfma_f32_16x16x32_bf16 v[80:83], v[140:143], v[206:209], v[80:83]
	v_mfma_f32_16x16x32_bf16 v[80:83], v[136:139], v[202:205], v[80:83]
	s_barrier
	s_mov_b32 m0, s39
	ds_read_b128 v[168:171], v221 offset:49152
	ds_read_b128 v[172:175], v221 offset:50176
	ds_read_b128 v[176:179], v221 offset:51200
	ds_read_b128 v[180:183], v221 offset:52224
	ds_read_b128 v[184:187], v221 offset:53248
	ds_read_b128 v[188:191], v221 offset:54272
	ds_read_b128 v[202:205], v221 offset:55296
	ds_read_b128 v[206:209], v221 offset:56320
	s_add_u32 s70, s46, s78
	s_addc_u32 s71, s47, s79
	global_load_lds_dwordx4 v194, s[70:71]
	s_mov_b32 m0, s40
	s_nop 0
	s_add_u32 s70, s46, s84
	s_addc_u32 s71, s47, s85
	global_load_lds_dwordx4 v194, s[70:71]
	s_mov_b32 m0, s41
	s_add_u32 s70, s46, s50
	s_addc_u32 s71, s47, s51
	global_load_lds_dwordx4 v194, s[70:71]
	s_mov_b32 m0, s42
	s_nop 0
	s_add_u32 s70, s46, s54
	s_addc_u32 s71, s47, s55
	global_load_lds_dwordx4 v194, s[70:71]
	s_mov_b32 m0, s27
	s_nop 0
	s_add_u32 s70, s44, s78
	s_addc_u32 s71, s45, s79
	global_load_lds_dwordx4 v196, s[70:71]
	s_mov_b32 m0, s28
	s_nop 0
	s_add_u32 s70, s44, s92
	s_addc_u32 s71, s45, s93
	global_load_lds_dwordx4 v196, s[70:71]
	s_waitcnt vmcnt(8)
	s_waitcnt lgkmcnt(0)
	s_barrier
	v_mfma_f32_16x16x32_bf16 v[64:67], v[136:139], v[168:171], v[64:67]
	v_mfma_f32_16x16x32_bf16 v[64:67], v[140:143], v[172:175], v[64:67]
	v_mfma_f32_16x16x32_bf16 v[60:63], v[148:151], v[172:175], v[60:63]
	v_mfma_f32_16x16x32_bf16 v[60:63], v[144:147], v[168:171], v[60:63]
	v_mfma_f32_16x16x32_bf16 v[56:59], v[152:155], v[168:171], v[56:59]
	v_mfma_f32_16x16x32_bf16 v[56:59], v[156:159], v[172:175], v[56:59]
	v_mfma_f32_16x16x32_bf16 v[52:55], v[164:167], v[172:175], v[52:55]
	v_mfma_f32_16x16x32_bf16 v[52:55], v[160:163], v[168:171], v[52:55]
	v_mfma_f32_16x16x32_bf16 v[36:39], v[160:163], v[176:179], v[36:39]
	v_mfma_f32_16x16x32_bf16 v[36:39], v[164:167], v[180:183], v[36:39]
	v_mfma_f32_16x16x32_bf16 v[40:43], v[156:159], v[180:183], v[40:43]
	v_mfma_f32_16x16x32_bf16 v[40:43], v[152:155], v[176:179], v[40:43]
	v_mfma_f32_16x16x32_bf16 v[44:47], v[144:147], v[176:179], v[44:47]
	v_mfma_f32_16x16x32_bf16 v[44:47], v[148:151], v[180:183], v[44:47]
	v_mfma_f32_16x16x32_bf16 v[48:51], v[140:143], v[180:183], v[48:51]
	v_mfma_f32_16x16x32_bf16 v[48:51], v[136:139], v[176:179], v[48:51]
	v_mfma_f32_16x16x32_bf16 v[32:35], v[136:139], v[184:187], v[32:35]
	v_mfma_f32_16x16x32_bf16 v[32:35], v[140:143], v[188:191], v[32:35]
	v_mfma_f32_16x16x32_bf16 v[28:31], v[148:151], v[188:191], v[28:31]
	v_mfma_f32_16x16x32_bf16 v[28:31], v[144:147], v[184:187], v[28:31]
	v_mfma_f32_16x16x32_bf16 v[24:27], v[152:155], v[184:187], v[24:27]
	v_mfma_f32_16x16x32_bf16 v[24:27], v[156:159], v[188:191], v[24:27]
	v_mfma_f32_16x16x32_bf16 v[20:23], v[164:167], v[188:191], v[20:23]
	v_mfma_f32_16x16x32_bf16 v[20:23], v[160:163], v[184:187], v[20:23]
	v_mfma_f32_16x16x32_bf16 v[4:7], v[160:163], v[202:205], v[4:7]
	v_mfma_f32_16x16x32_bf16 v[4:7], v[164:167], v[206:209], v[4:7]
	v_mfma_f32_16x16x32_bf16 v[8:11], v[156:159], v[206:209], v[8:11]
	v_mfma_f32_16x16x32_bf16 v[8:11], v[152:155], v[202:205], v[8:11]
	v_mfma_f32_16x16x32_bf16 v[12:15], v[144:147], v[202:205], v[12:15]
	v_mfma_f32_16x16x32_bf16 v[12:15], v[148:151], v[206:209], v[12:15]
	v_mfma_f32_16x16x32_bf16 v[16:19], v[140:143], v[206:209], v[16:19]
	v_mfma_f32_16x16x32_bf16 v[16:19], v[136:139], v[202:205], v[16:19]
	s_barrier
	s_add_i32 s15, s15, 2
	s_add_u32 s20, s20, 0x100
	s_addc_u32 s21, s21, 0
	s_add_u32 s8, s8, 0x100
	s_addc_u32 s9, s9, 0
	s_cmp_gt_u32 s15, 29
	s_cbranch_scc0 .LBB0_594
	s_and_b64 vcc, exec, s[12:13]
	s_cbranch_vccz .LBB0_597
	s_barrier

.LBB0_700:
	ds_read_b128 v[120:123], v116
	ds_read_b128 v[132:135], v116 offset:1024
	ds_read_b128 v[144:147], v116 offset:2048
	ds_read_b128 v[148:151], v116 offset:3072
	ds_read_b128 v[152:155], v117
	ds_read_b128 v[156:159], v117 offset:1024
	ds_read_b128 v[166:169], v117 offset:2048
	ds_read_b128 v[170:173], v117 offset:3072
	s_add_u32 s27, s10, 0xfff7c080
	s_addc_u32 s47, s11, -1
	s_cmp_eq_u32 s26, 28
	s_cselect_b32 s49, s21, s47
	s_cselect_b32 s48, s20, s27
	s_cselect_b32 s51, s3, s25
	s_cselect_b32 s50, s4, s24
	s_mov_b32 m0, s5
	ds_read_b128 v[180:183], v178
	ds_read_b128 v[184:187], v178 offset:1024
	ds_read_b128 v[188:191], v178 offset:2048
	ds_read_b128 v[192:195], v178 offset:3072
	ds_read_b128 v[196:199], v178 offset:4096
	ds_read_b128 v[200:203], v178 offset:5120
	ds_read_b128 v[204:207], v178 offset:6144
	ds_read_b128 v[214:217], v178 offset:7168
	global_load_lds_dwordx4 v164, s[10:11]
	s_mov_b32 m0, s19
	s_nop 0
	s_add_u32 s70, s10, s96
	s_addc_u32 s71, s11, s97
	global_load_lds_dwordx4 v164, s[70:71]
	s_waitcnt vmcnt(8)
	s_waitcnt lgkmcnt(0)
	s_barrier
	v_mfma_f32_16x16x32_bf16 v[140:143], v[120:123], v[180:183], v[140:143]
	v_mfma_f32_16x16x32_bf16 v[140:143], v[132:135], v[184:187], v[140:143]
	v_mfma_f32_16x16x32_bf16 v[136:139], v[148:151], v[184:187], v[136:139]
	v_mfma_f32_16x16x32_bf16 v[136:139], v[144:147], v[180:183], v[136:139]
	v_mfma_f32_16x16x32_bf16 v[128:131], v[152:155], v[180:183], v[128:131]
	v_mfma_f32_16x16x32_bf16 v[128:131], v[156:159], v[184:187], v[128:131]
	v_mfma_f32_16x16x32_bf16 v[124:127], v[170:173], v[184:187], v[124:127]
	v_mfma_f32_16x16x32_bf16 v[124:127], v[166:169], v[180:183], v[124:127]
	v_mfma_f32_16x16x32_bf16 v[100:103], v[166:169], v[188:191], v[100:103]
	v_mfma_f32_16x16x32_bf16 v[100:103], v[170:173], v[192:195], v[100:103]
	v_mfma_f32_16x16x32_bf16 v[104:107], v[156:159], v[192:195], v[104:107]
	v_mfma_f32_16x16x32_bf16 v[104:107], v[152:155], v[188:191], v[104:107]
	v_mfma_f32_16x16x32_bf16 v[108:111], v[144:147], v[188:191], v[108:111]
	v_mfma_f32_16x16x32_bf16 v[108:111], v[148:151], v[192:195], v[108:111]
	v_mfma_f32_16x16x32_bf16 v[112:115], v[132:135], v[192:195], v[112:115]
	v_mfma_f32_16x16x32_bf16 v[112:115], v[120:123], v[188:191], v[112:115]
	v_mfma_f32_16x16x32_bf16 v[96:99], v[120:123], v[196:199], v[96:99]
	v_mfma_f32_16x16x32_bf16 v[96:99], v[132:135], v[200:203], v[96:99]
	v_mfma_f32_16x16x32_bf16 v[92:95], v[148:151], v[200:203], v[92:95]
	v_mfma_f32_16x16x32_bf16 v[92:95], v[144:147], v[196:199], v[92:95]
	v_mfma_f32_16x16x32_bf16 v[88:91], v[152:155], v[196:199], v[88:91]
	v_mfma_f32_16x16x32_bf16 v[88:91], v[156:159], v[200:203], v[88:91]
	v_mfma_f32_16x16x32_bf16 v[84:87], v[170:173], v[200:203], v[84:87]
	v_mfma_f32_16x16x32_bf16 v[84:87], v[166:169], v[196:199], v[84:87]
	v_mfma_f32_16x16x32_bf16 v[68:71], v[166:169], v[204:207], v[68:71]
	v_mfma_f32_16x16x32_bf16 v[68:71], v[170:173], v[214:217], v[68:71]
	v_mfma_f32_16x16x32_bf16 v[72:75], v[156:159], v[214:217], v[72:75]
	v_mfma_f32_16x16x32_bf16 v[72:75], v[152:155], v[204:207], v[72:75]
	v_mfma_f32_16x16x32_bf16 v[76:79], v[144:147], v[204:207], v[76:79]
	v_mfma_f32_16x16x32_bf16 v[76:79], v[148:151], v[214:217], v[76:79]
	v_mfma_f32_16x16x32_bf16 v[80:83], v[132:135], v[214:217], v[80:83]
	v_mfma_f32_16x16x32_bf16 v[80:83], v[120:123], v[204:207], v[80:83]
	s_barrier
	s_mov_b32 m0, s33
	ds_read_b128 v[180:183], v178 offset:16384
	ds_read_b128 v[184:187], v178 offset:17408
	ds_read_b128 v[188:191], v178 offset:18432
	ds_read_b128 v[192:195], v178 offset:19456
	ds_read_b128 v[196:199], v178 offset:20480
	ds_read_b128 v[200:203], v178 offset:21504
	ds_read_b128 v[204:207], v178 offset:22528
	ds_read_b128 v[214:217], v178 offset:23552
	global_load_lds_dwordx4 v160, s[50:51]
	s_mov_b32 m0, s40
	s_nop 0
	s_add_u32 s70, s50, s90
	s_addc_u32 s71, s51, s91
	global_load_lds_dwordx4 v160, s[70:71]
	s_mov_b32 m0, s41
	s_nop 0
	s_add_u32 s70, s50, s52
	s_addc_u32 s71, s51, s53
	global_load_lds_dwordx4 v160, s[70:71]
	s_mov_b32 m0, s42
	s_nop 0
	s_add_u32 s70, s50, s56
	s_addc_u32 s71, s51, s57
	global_load_lds_dwordx4 v160, s[70:71]
	s_mov_b32 m0, s29
	s_nop 0
	global_load_lds_dwordx4 v162, s[48:49]
	s_mov_b32 m0, s30
	s_nop 0
	s_add_u32 s70, s48, s96
	s_addc_u32 s71, s49, s97
	global_load_lds_dwordx4 v162, s[70:71]
	s_waitcnt vmcnt(8)
	s_waitcnt lgkmcnt(0)
	s_barrier
	v_mfma_f32_16x16x32_bf16 v[56:59], v[120:123], v[180:183], v[56:59]
	v_mfma_f32_16x16x32_bf16 v[56:59], v[132:135], v[184:187], v[56:59]
	v_mfma_f32_16x16x32_bf16 v[52:55], v[148:151], v[184:187], v[52:55]
	v_mfma_f32_16x16x32_bf16 v[52:55], v[144:147], v[180:183], v[52:55]
	v_mfma_f32_16x16x32_bf16 v[64:67], v[152:155], v[180:183], v[64:67]
	v_mfma_f32_16x16x32_bf16 v[64:67], v[156:159], v[184:187], v[64:67]
	v_mfma_f32_16x16x32_bf16 v[60:63], v[170:173], v[184:187], v[60:63]
	v_mfma_f32_16x16x32_bf16 v[60:63], v[166:169], v[180:183], v[60:63]
	v_mfma_f32_16x16x32_bf16 v[36:39], v[166:169], v[188:191], v[36:39]
	v_mfma_f32_16x16x32_bf16 v[36:39], v[170:173], v[192:195], v[36:39]
	v_mfma_f32_16x16x32_bf16 v[40:43], v[156:159], v[192:195], v[40:43]
	v_mfma_f32_16x16x32_bf16 v[40:43], v[152:155], v[188:191], v[40:43]
	v_mfma_f32_16x16x32_bf16 v[44:47], v[144:147], v[188:191], v[44:47]
	v_mfma_f32_16x16x32_bf16 v[44:47], v[148:151], v[192:195], v[44:47]
	v_mfma_f32_16x16x32_bf16 v[48:51], v[132:135], v[192:195], v[48:51]
	v_mfma_f32_16x16x32_bf16 v[48:51], v[120:123], v[188:191], v[48:51]
	v_mfma_f32_16x16x32_bf16 v[32:35], v[120:123], v[196:199], v[32:35]
	v_mfma_f32_16x16x32_bf16 v[32:35], v[132:135], v[200:203], v[32:35]
	v_mfma_f32_16x16x32_bf16 v[28:31], v[148:151], v[200:203], v[28:31]
	v_mfma_f32_16x16x32_bf16 v[28:31], v[144:147], v[196:199], v[28:31]
	v_mfma_f32_16x16x32_bf16 v[24:27], v[152:155], v[196:199], v[24:27]
	v_mfma_f32_16x16x32_bf16 v[24:27], v[156:159], v[200:203], v[24:27]
	v_mfma_f32_16x16x32_bf16 v[20:23], v[170:173], v[200:203], v[20:23]
	v_mfma_f32_16x16x32_bf16 v[20:23], v[166:169], v[196:199], v[20:23]
	v_mfma_f32_16x16x32_bf16 v[4:7], v[166:169], v[204:207], v[4:7]
	v_mfma_f32_16x16x32_bf16 v[4:7], v[170:173], v[214:217], v[4:7]
	v_mfma_f32_16x16x32_bf16 v[8:11], v[156:159], v[214:217], v[8:11]
	v_mfma_f32_16x16x32_bf16 v[8:11], v[152:155], v[204:207], v[8:11]
	v_mfma_f32_16x16x32_bf16 v[12:15], v[144:147], v[204:207], v[12:15]
	v_mfma_f32_16x16x32_bf16 v[12:15], v[148:151], v[214:217], v[12:15]
	v_mfma_f32_16x16x32_bf16 v[16:19], v[132:135], v[214:217], v[16:19]
	v_mfma_f32_16x16x32_bf16 v[16:19], v[120:123], v[204:207], v[16:19]
	s_barrier
; #define PG8_MMA(ai, bj, At, Bt) do { __builtin_amdgcn_s_setprio(1); _Pragma("unroll") for (int m = 0; m < 4; ++m) _Pragma("unroll") for (int n = 0; n < 2; ++n) _Pragma("unroll") for (int k = 0; k < 2; ++k) \
;         acc[ai][bj][m][n] = __builtin_amdgcn_mfma_f32_16x16x32_bf16(Bt[n][k], At[m][k], acc[ai][bj][m][n], 0, 0, 0); __builtin_amdgcn_s_setprio(0); } while (0)
; #define PG8_WAIT_V(n) asm volatile("s_waitcnt vmcnt(" #n ")" ::: "memory")
; #define PG8_TRIP_HEAD(T) const int t = (T); const bool last = (t == nt - 2); \
;             const char* a1 = cA + (size_t)(t + 1) * kstep; \
;             const char* a2 = last ? nA : cA + (size_t)(t + 2) * kstep; const char* b2 = last ? nB : cB + (size_t)(t + 2) * kstep; \
;             const char* a3 = a2 + kstep; const char* b3 = b2 + kstep; \
;             if (last && has_next) S.a_ready(nxt);
; template <class Epi, class Sched, bool ALIGN_EPI = false, bool SP2 = false>
; __device__ __forceinline__ void gemm_phase(PG8_LAS unsigned char* lds, const Gemm g, const Sched& S, const Epi& E) {
;     ...
;         if constexpr (SP2) {
;             { PG8_TRIP_HEAD(0) PG8_TRIP_SP2(asm volatile("s_waitcnt vmcnt(%0)" :: "n"(8 + Epi::NST) : "memory"), PG8_MMAZ) }
;             for (int tt = 2; tt < nt; tt += 2) { PG8_TRIP_HEAD(tt) PG8_TRIP_SP2(PG8_WAIT_V(8), PG8_MMA) }
	ds_read_b128 v[120:123], v118
	ds_read_b128 v[132:135], v118 offset:1024
	ds_read_b128 v[144:147], v118 offset:2048
	ds_read_b128 v[148:151], v118 offset:3072
	ds_read_b128 v[152:155], v119
	ds_read_b128 v[156:159], v119 offset:1024
	ds_read_b128 v[166:169], v119 offset:2048
	ds_read_b128 v[170:173], v119 offset:3072
	s_mov_b32 m0, s31
	ds_read_b128 v[180:183], v178 offset:32768
	ds_read_b128 v[184:187], v178 offset:33792
	ds_read_b128 v[188:191], v178 offset:34816
	ds_read_b128 v[192:195], v178 offset:35840
	ds_read_b128 v[196:199], v178 offset:36864
	ds_read_b128 v[200:203], v178 offset:37888
	ds_read_b128 v[204:207], v178 offset:38912
	ds_read_b128 v[214:217], v178 offset:39936
	s_add_u32 s70, s48, s82
	s_addc_u32 s71, s49, s83
	global_load_lds_dwordx4 v162, s[70:71]
	s_mov_b32 m0, s34
	s_nop 0
	s_add_u32 s70, s48, s62
	s_addc_u32 s71, s49, s63
	global_load_lds_dwordx4 v162, s[70:71]
	s_waitcnt vmcnt(8)
	s_waitcnt lgkmcnt(0)
	s_barrier
	v_mfma_f32_16x16x32_bf16 v[140:143], v[120:123], v[180:183], v[140:143]
	v_mfma_f32_16x16x32_bf16 v[140:143], v[132:135], v[184:187], v[140:143]
	v_mfma_f32_16x16x32_bf16 v[136:139], v[148:151], v[184:187], v[136:139]
	v_mfma_f32_16x16x32_bf16 v[136:139], v[144:147], v[180:183], v[136:139]
	v_mfma_f32_16x16x32_bf16 v[128:131], v[152:155], v[180:183], v[128:131]
	v_mfma_f32_16x16x32_bf16 v[128:131], v[156:159], v[184:187], v[128:131]
	v_mfma_f32_16x16x32_bf16 v[124:127], v[170:173], v[184:187], v[124:127]
	v_mfma_f32_16x16x32_bf16 v[124:127], v[166:169], v[180:183], v[124:127]
	v_mfma_f32_16x16x32_bf16 v[100:103], v[166:169], v[188:191], v[100:103]
	v_mfma_f32_16x16x32_bf16 v[100:103], v[170:173], v[192:195], v[100:103]
	v_mfma_f32_16x16x32_bf16 v[104:107], v[156:159], v[192:195], v[104:107]
	v_mfma_f32_16x16x32_bf16 v[104:107], v[152:155], v[188:191], v[104:107]
	v_mfma_f32_16x16x32_bf16 v[108:111], v[144:147], v[188:191], v[108:111]
	v_mfma_f32_16x16x32_bf16 v[108:111], v[148:151], v[192:195], v[108:111]
	v_mfma_f32_16x16x32_bf16 v[112:115], v[132:135], v[192:195], v[112:115]
	v_mfma_f32_16x16x32_bf16 v[112:115], v[120:123], v[188:191], v[112:115]
	v_mfma_f32_16x16x32_bf16 v[96:99], v[120:123], v[196:199], v[96:99]
	v_mfma_f32_16x16x32_bf16 v[96:99], v[132:135], v[200:203], v[96:99]
	v_mfma_f32_16x16x32_bf16 v[92:95], v[148:151], v[200:203], v[92:95]
	v_mfma_f32_16x16x32_bf16 v[92:95], v[144:147], v[196:199], v[92:95]
	v_mfma_f32_16x16x32_bf16 v[88:91], v[152:155], v[196:199], v[88:91]
	v_mfma_f32_16x16x32_bf16 v[88:91], v[156:159], v[200:203], v[88:91]
	v_mfma_f32_16x16x32_bf16 v[84:87], v[170:173], v[200:203], v[84:87]
	v_mfma_f32_16x16x32_bf16 v[84:87], v[166:169], v[196:199], v[84:87]
	v_mfma_f32_16x16x32_bf16 v[68:71], v[166:169], v[204:207], v[68:71]
	v_mfma_f32_16x16x32_bf16 v[68:71], v[170:173], v[214:217], v[68:71]
	v_mfma_f32_16x16x32_bf16 v[72:75], v[156:159], v[214:217], v[72:75]
	v_mfma_f32_16x16x32_bf16 v[72:75], v[152:155], v[204:207], v[72:75]
	v_mfma_f32_16x16x32_bf16 v[76:79], v[144:147], v[204:207], v[76:79]
	v_mfma_f32_16x16x32_bf16 v[76:79], v[148:151], v[214:217], v[76:79]
	v_mfma_f32_16x16x32_bf16 v[80:83], v[132:135], v[214:217], v[80:83]
	v_mfma_f32_16x16x32_bf16 v[80:83], v[120:123], v[204:207], v[80:83]
	s_barrier
	s_mov_b32 m0, s43
	ds_read_b128 v[180:183], v178 offset:49152
	ds_read_b128 v[184:187], v178 offset:50176
	ds_read_b128 v[188:191], v178 offset:51200
	ds_read_b128 v[192:195], v178 offset:52224
	ds_read_b128 v[196:199], v178 offset:53248
	ds_read_b128 v[200:203], v178 offset:54272
	ds_read_b128 v[204:207], v178 offset:55296
	ds_read_b128 v[214:217], v178 offset:56320
	s_add_u32 s70, s50, s78
	s_addc_u32 s71, s51, s79
	global_load_lds_dwordx4 v160, s[70:71]
	s_mov_b32 m0, s44
	s_nop 0
	s_add_u32 s70, s50, s84
	s_addc_u32 s71, s51, s85
	global_load_lds_dwordx4 v160, s[70:71]
	s_mov_b32 m0, s45
	s_add_u32 s70, s50, s54
	s_addc_u32 s71, s51, s55
	global_load_lds_dwordx4 v160, s[70:71]
	s_mov_b32 m0, s46
	s_nop 0
	s_add_u32 s70, s50, s60
	s_addc_u32 s71, s51, s61
	global_load_lds_dwordx4 v160, s[70:71]
	s_mov_b32 m0, s36
	s_nop 0
	s_add_u32 s70, s48, s78
	s_addc_u32 s71, s49, s79
	global_load_lds_dwordx4 v162, s[70:71]
	s_mov_b32 m0, s37
	s_nop 0
	s_add_u32 s70, s48, s92
	s_addc_u32 s71, s49, s93
	global_load_lds_dwordx4 v162, s[70:71]
	s_waitcnt vmcnt(8)
	s_waitcnt lgkmcnt(0)
	s_barrier
	v_mfma_f32_16x16x32_bf16 v[56:59], v[120:123], v[180:183], v[56:59]
	v_mfma_f32_16x16x32_bf16 v[56:59], v[132:135], v[184:187], v[56:59]
	v_mfma_f32_16x16x32_bf16 v[52:55], v[148:151], v[184:187], v[52:55]
	v_mfma_f32_16x16x32_bf16 v[52:55], v[144:147], v[180:183], v[52:55]
	v_mfma_f32_16x16x32_bf16 v[64:67], v[152:155], v[180:183], v[64:67]
	v_mfma_f32_16x16x32_bf16 v[64:67], v[156:159], v[184:187], v[64:67]
	v_mfma_f32_16x16x32_bf16 v[60:63], v[170:173], v[184:187], v[60:63]
	v_mfma_f32_16x16x32_bf16 v[60:63], v[166:169], v[180:183], v[60:63]
	v_mfma_f32_16x16x32_bf16 v[36:39], v[166:169], v[188:191], v[36:39]
	v_mfma_f32_16x16x32_bf16 v[36:39], v[170:173], v[192:195], v[36:39]
	v_mfma_f32_16x16x32_bf16 v[40:43], v[156:159], v[192:195], v[40:43]
	v_mfma_f32_16x16x32_bf16 v[40:43], v[152:155], v[188:191], v[40:43]
	v_mfma_f32_16x16x32_bf16 v[44:47], v[144:147], v[188:191], v[44:47]
	v_mfma_f32_16x16x32_bf16 v[44:47], v[148:151], v[192:195], v[44:47]
	v_mfma_f32_16x16x32_bf16 v[48:51], v[132:135], v[192:195], v[48:51]
	v_mfma_f32_16x16x32_bf16 v[48:51], v[120:123], v[188:191], v[48:51]
	v_mfma_f32_16x16x32_bf16 v[32:35], v[120:123], v[196:199], v[32:35]
	v_mfma_f32_16x16x32_bf16 v[32:35], v[132:135], v[200:203], v[32:35]
	v_mfma_f32_16x16x32_bf16 v[28:31], v[148:151], v[200:203], v[28:31]
	v_mfma_f32_16x16x32_bf16 v[28:31], v[144:147], v[196:199], v[28:31]
	v_mfma_f32_16x16x32_bf16 v[24:27], v[152:155], v[196:199], v[24:27]
	v_mfma_f32_16x16x32_bf16 v[24:27], v[156:159], v[200:203], v[24:27]
	v_mfma_f32_16x16x32_bf16 v[20:23], v[170:173], v[200:203], v[20:23]
	v_mfma_f32_16x16x32_bf16 v[20:23], v[166:169], v[196:199], v[20:23]
	v_mfma_f32_16x16x32_bf16 v[4:7], v[166:169], v[204:207], v[4:7]
	v_mfma_f32_16x16x32_bf16 v[4:7], v[170:173], v[214:217], v[4:7]
	v_mfma_f32_16x16x32_bf16 v[8:11], v[156:159], v[214:217], v[8:11]
	v_mfma_f32_16x16x32_bf16 v[8:11], v[152:155], v[204:207], v[8:11]
	v_mfma_f32_16x16x32_bf16 v[12:15], v[144:147], v[204:207], v[12:15]
	v_mfma_f32_16x16x32_bf16 v[12:15], v[148:151], v[214:217], v[12:15]
	v_mfma_f32_16x16x32_bf16 v[16:19], v[132:135], v[214:217], v[16:19]
	v_mfma_f32_16x16x32_bf16 v[16:19], v[120:123], v[204:207], v[16:19]
	s_barrier
	s_add_i32 s26, s26, 2
	s_add_u32 s10, s10, 0x100
	s_addc_u32 s11, s11, 0
	s_add_u32 s24, s24, 0x100
	s_addc_u32 s25, s25, 0
	s_cmp_gt_u32 s26, 29
	s_cbranch_scc0 .LBB0_700
	s_and_b64 vcc, exec, s[16:17]
	s_cbranch_vccz .LBB0_703
	s_barrier
